# v023
# speedup vs baseline: 1.0914x; 1.0188x over previous
.LBB2_45:
	s_and_b64 vcc, exec, s[28:29]
	s_cbranch_vccnz .Lmy_epi_last
	s_cmp_eq_u32 s30, 7
	s_cbranch_scc1 .Lmy_epi_nl7
	v_exp_f32_e32 v120, v120
	v_exp_f32_e32 v121, v121
	v_exp_f32_e32 v122, v122
	v_pk_add_f32 v[120:121], v[120:121], 1.0 op_sel_hi:[1,0]
	v_exp_f32_e32 v123, v123
	v_exp_f32_e32 v124, v124
	v_pk_add_f32 v[122:123], v[122:123], 1.0 op_sel_hi:[1,0]
	v_exp_f32_e32 v125, v125
	v_exp_f32_e32 v126, v126
	v_pk_add_f32 v[124:125], v[124:125], 1.0 op_sel_hi:[1,0]
	v_exp_f32_e32 v127, v127
	v_exp_f32_e32 v116, v116
	v_pk_add_f32 v[126:127], v[126:127], 1.0 op_sel_hi:[1,0]
	v_exp_f32_e32 v117, v117
	v_pk_mul_f32 v[120:121], v[120:121], v[124:125]
	v_exp_f32_e32 v118, v118
	v_pk_mul_f32 v[122:123], v[122:123], v[126:127]
	v_exp_f32_e32 v119, v119
	v_pk_add_f32 v[116:117], v[116:117], 1.0 op_sel_hi:[1,0]
	v_rcp_f32_e32 v120, v120
	v_rcp_f32_e32 v121, v121
	v_pk_add_f32 v[118:119], v[118:119], 1.0 op_sel_hi:[1,0]
	v_rcp_f32_e32 v122, v122
	v_rcp_f32_e32 v123, v123
	v_pk_add_f32 v[124:125], v[124:125], 2.0 op_sel_hi:[1,0] neg_lo:[1,0] neg_hi:[1,0]
	v_rcp_f32_e32 v116, v116
	v_rcp_f32_e32 v117, v117
	v_pk_add_f32 v[126:127], v[126:127], 2.0 op_sel_hi:[1,0] neg_lo:[1,0] neg_hi:[1,0]
	v_rcp_f32_e32 v118, v118
	v_rcp_f32_e32 v119, v119
	v_pk_mul_f32 v[124:125], v[124:125], v[120:121]
	v_pk_mul_f32 v[126:127], v[126:127], v[122:123]
	s_waitcnt lgkmcnt(3)
	v_pk_fma_f32 v[116:117], v[172:173], v[116:117], v[124:125]
	v_pk_fma_f32 v[118:119], v[174:175], v[118:119], v[126:127]
	global_store_dwordx4 v[176:177], v[116:119], off nt
	s_nop 1
	v_pk_mul_f32 v[116:117], v[116:117], s[96:97] op_sel_hi:[1,0]
	v_pk_mul_f32 v[118:119], v[118:119], s[96:97] op_sel_hi:[1,0]
	v_exp_f32_e32 v112, v112
	v_exp_f32_e32 v113, v113
	v_exp_f32_e32 v114, v114
	v_pk_fma_f32 v[112:113], v[112:113], s[98:99], s[98:99] op_sel_hi:[1,0,0]
	v_exp_f32_e32 v115, v115
	v_exp_f32_e32 v116, v116
	v_pk_fma_f32 v[114:115], v[114:115], s[98:99], s[98:99] op_sel_hi:[1,0,0]
	v_exp_f32_e32 v117, v117
	v_exp_f32_e32 v118, v118
	v_pk_add_f32 v[116:117], v[116:117], 1.0 op_sel_hi:[1,0]
	v_exp_f32_e32 v119, v119
	v_pk_mul_f32 v[112:113], v[112:113], v[116:117]
	v_rcp_f32_e32 v112, v112
	v_pk_add_f32 v[118:119], v[118:119], 1.0 op_sel_hi:[1,0]
	v_rcp_f32_e32 v113, v113
	v_pk_mul_f32 v[114:115], v[114:115], v[118:119]
	v_pk_add_f32 v[116:117], v[116:117], 2.0 op_sel_hi:[1,0] neg_lo:[1,0] neg_hi:[1,0]
	v_rcp_f32_e32 v114, v114
	v_rcp_f32_e32 v115, v115
	v_pk_add_f32 v[118:119], v[118:119], 2.0 op_sel_hi:[1,0] neg_lo:[1,0] neg_hi:[1,0]
	v_pk_mul_f32 v[112:113], v[112:113], v[116:117]
	v_pk_mul_f32 v[114:115], v[114:115], v[118:119]
	v_cvt_pk_fp8_f32 v124, v112, v113
	s_add_u32 s0, s8, s27
	s_addc_u32 s1, s9, 0
	s_ashr_i32 s35, s34, 31
	s_lshl_b64 s[34:35], s[34:35], 21
	v_ashrrev_i32_e32 v209, 31, v208
	s_add_u32 s36, s73, s34
	v_lshl_add_u64 v[122:123], s[0:1], 0, v[210:211]
	v_cvt_pk_fp8_f32 v124, v114, v115 op_sel:[0,0,1]
	v_lshlrev_b64 v[116:117], 10, v[208:209]
	s_addc_u32 s37, s74, s35
	v_lshl_add_u64 v[118:119], v[122:123], 0, v[116:117]
	global_store_dword v[118:119], v124, off
	s_cmp_eq_u32 s30, 7
	s_cselect_b64 s[34:35], -1, 0
	s_cmp_lg_u32 s30, 7
	v_lshl_add_u64 v[120:121], v[210:211], 1, s[36:37]
	v_exp_f32_e32 v104, v104
	v_exp_f32_e32 v105, v105
	v_exp_f32_e32 v106, v106
	v_pk_add_f32 v[104:105], v[104:105], 1.0 op_sel_hi:[1,0]
	v_exp_f32_e32 v107, v107
	v_exp_f32_e32 v108, v108
	v_pk_add_f32 v[106:107], v[106:107], 1.0 op_sel_hi:[1,0]
	v_exp_f32_e32 v109, v109
	v_exp_f32_e32 v110, v110
	v_pk_add_f32 v[108:109], v[108:109], 1.0 op_sel_hi:[1,0]
	v_exp_f32_e32 v111, v111
	v_exp_f32_e32 v100, v100
	v_pk_add_f32 v[110:111], v[110:111], 1.0 op_sel_hi:[1,0]
	v_exp_f32_e32 v101, v101
	v_pk_mul_f32 v[104:105], v[104:105], v[108:109]
	v_exp_f32_e32 v102, v102
	v_pk_mul_f32 v[106:107], v[106:107], v[110:111]
	v_exp_f32_e32 v103, v103
	v_pk_add_f32 v[100:101], v[100:101], 1.0 op_sel_hi:[1,0]
	v_rcp_f32_e32 v104, v104
	v_rcp_f32_e32 v105, v105
	v_pk_add_f32 v[102:103], v[102:103], 1.0 op_sel_hi:[1,0]
	v_rcp_f32_e32 v106, v106
	v_rcp_f32_e32 v107, v107
	v_pk_add_f32 v[108:109], v[108:109], 2.0 op_sel_hi:[1,0] neg_lo:[1,0] neg_hi:[1,0]
	v_rcp_f32_e32 v100, v100
	v_rcp_f32_e32 v101, v101
	v_pk_add_f32 v[110:111], v[110:111], 2.0 op_sel_hi:[1,0] neg_lo:[1,0] neg_hi:[1,0]
	v_rcp_f32_e32 v102, v102
	v_rcp_f32_e32 v103, v103
	v_pk_mul_f32 v[108:109], v[108:109], v[104:105]
	v_pk_mul_f32 v[110:111], v[110:111], v[106:107]
	s_waitcnt lgkmcnt(2)
	v_lshl_add_u64 v[104:105], v[176:177], 0, s[18:19]
	v_pk_fma_f32 v[100:101], v[168:169], v[100:101], v[108:109]
	v_pk_fma_f32 v[102:103], v[170:171], v[102:103], v[110:111]
	global_store_dwordx4 v[104:105], v[100:103], off nt
	s_nop 1
	v_pk_mul_f32 v[100:101], v[100:101], s[96:97] op_sel_hi:[1,0]
	v_pk_mul_f32 v[102:103], v[102:103], s[96:97] op_sel_hi:[1,0]
	v_exp_f32_e32 v96, v96
	v_exp_f32_e32 v97, v97
	v_exp_f32_e32 v98, v98
	v_pk_fma_f32 v[96:97], v[96:97], s[98:99], s[98:99] op_sel_hi:[1,0,0]
	v_exp_f32_e32 v99, v99
	v_exp_f32_e32 v100, v100
	v_pk_fma_f32 v[98:99], v[98:99], s[98:99], s[98:99] op_sel_hi:[1,0,0]
	v_exp_f32_e32 v101, v101
	v_exp_f32_e32 v102, v102
	v_pk_add_f32 v[100:101], v[100:101], 1.0 op_sel_hi:[1,0]
	v_exp_f32_e32 v103, v103
	v_pk_mul_f32 v[96:97], v[96:97], v[100:101]
	v_rcp_f32_e32 v96, v96
	v_pk_add_f32 v[102:103], v[102:103], 1.0 op_sel_hi:[1,0]
	v_rcp_f32_e32 v97, v97
	v_pk_mul_f32 v[98:99], v[98:99], v[102:103]
	v_pk_add_f32 v[100:101], v[100:101], 2.0 op_sel_hi:[1,0] neg_lo:[1,0] neg_hi:[1,0]
	v_rcp_f32_e32 v98, v98
	v_rcp_f32_e32 v99, v99
	v_pk_add_f32 v[102:103], v[102:103], 2.0 op_sel_hi:[1,0] neg_lo:[1,0] neg_hi:[1,0]
	v_pk_mul_f32 v[96:97], v[96:97], v[100:101]
	v_pk_mul_f32 v[98:99], v[98:99], v[102:103]
	v_cvt_pk_fp8_f32 v104, v96, v97
	v_ashrrev_i32_e32 v207, 31, v206
	v_lshlrev_b64 v[100:101], 10, v[206:207]
	v_lshl_add_u64 v[102:103], v[122:123], 0, v[100:101]
	v_cvt_pk_fp8_f32 v104, v98, v99 op_sel:[0,0,1]
	v_cndmask_b32_e64 v105, 0, 1, s[34:35]
	global_store_dword v[102:103], v104, off
	v_cmp_ne_u32_e64 s[0:1], 1, v105
	v_exp_f32_e32 v88, v88
	v_exp_f32_e32 v89, v89
	v_exp_f32_e32 v90, v90
	v_pk_add_f32 v[88:89], v[88:89], 1.0 op_sel_hi:[1,0]
	v_exp_f32_e32 v91, v91
	v_exp_f32_e32 v92, v92
	v_pk_add_f32 v[90:91], v[90:91], 1.0 op_sel_hi:[1,0]
	v_exp_f32_e32 v93, v93
	v_exp_f32_e32 v94, v94
	v_pk_add_f32 v[92:93], v[92:93], 1.0 op_sel_hi:[1,0]
	v_exp_f32_e32 v95, v95
	v_exp_f32_e32 v84, v84
	v_pk_add_f32 v[94:95], v[94:95], 1.0 op_sel_hi:[1,0]
	v_exp_f32_e32 v85, v85
	v_pk_mul_f32 v[88:89], v[88:89], v[92:93]
	v_exp_f32_e32 v86, v86
	v_pk_mul_f32 v[90:91], v[90:91], v[94:95]
	v_exp_f32_e32 v87, v87
	v_pk_add_f32 v[84:85], v[84:85], 1.0 op_sel_hi:[1,0]
	v_rcp_f32_e32 v88, v88
	v_rcp_f32_e32 v89, v89
	v_pk_add_f32 v[86:87], v[86:87], 1.0 op_sel_hi:[1,0]
	v_rcp_f32_e32 v90, v90
	v_rcp_f32_e32 v91, v91
	v_pk_add_f32 v[92:93], v[92:93], 2.0 op_sel_hi:[1,0] neg_lo:[1,0] neg_hi:[1,0]
	v_rcp_f32_e32 v84, v84
	v_rcp_f32_e32 v85, v85
	v_pk_add_f32 v[94:95], v[94:95], 2.0 op_sel_hi:[1,0] neg_lo:[1,0] neg_hi:[1,0]
	v_rcp_f32_e32 v86, v86
	v_rcp_f32_e32 v87, v87
	v_pk_mul_f32 v[92:93], v[92:93], v[88:89]
	v_pk_mul_f32 v[94:95], v[94:95], v[90:91]
	s_waitcnt lgkmcnt(1)
	v_pk_fma_f32 v[84:85], v[164:165], v[84:85], v[92:93]
	v_pk_fma_f32 v[86:87], v[166:167], v[86:87], v[94:95]
	v_lshl_add_u64 v[88:89], v[176:177], 0, s[12:13]
	global_store_dwordx4 v[88:89], v[84:87], off nt
	s_nop 1
	v_pk_mul_f32 v[84:85], v[84:85], s[96:97] op_sel_hi:[1,0]
	v_pk_mul_f32 v[86:87], v[86:87], s[96:97] op_sel_hi:[1,0]
	v_exp_f32_e32 v80, v80
	v_exp_f32_e32 v81, v81
	v_exp_f32_e32 v82, v82
	v_pk_fma_f32 v[80:81], v[80:81], s[98:99], s[98:99] op_sel_hi:[1,0,0]
	v_exp_f32_e32 v83, v83
	v_exp_f32_e32 v84, v84
	v_pk_fma_f32 v[82:83], v[82:83], s[98:99], s[98:99] op_sel_hi:[1,0,0]
	v_exp_f32_e32 v85, v85
	v_exp_f32_e32 v86, v86
	v_pk_add_f32 v[84:85], v[84:85], 1.0 op_sel_hi:[1,0]
	v_exp_f32_e32 v87, v87
	v_pk_mul_f32 v[80:81], v[80:81], v[84:85]
	v_rcp_f32_e32 v80, v80
	v_pk_add_f32 v[86:87], v[86:87], 1.0 op_sel_hi:[1,0]
	v_rcp_f32_e32 v81, v81
	v_pk_mul_f32 v[82:83], v[82:83], v[86:87]
	v_pk_add_f32 v[84:85], v[84:85], 2.0 op_sel_hi:[1,0] neg_lo:[1,0] neg_hi:[1,0]
	v_rcp_f32_e32 v82, v82
	v_rcp_f32_e32 v83, v83
	v_pk_add_f32 v[86:87], v[86:87], 2.0 op_sel_hi:[1,0] neg_lo:[1,0] neg_hi:[1,0]
	v_pk_mul_f32 v[80:81], v[80:81], v[84:85]
	v_pk_mul_f32 v[82:83], v[82:83], v[86:87]
	v_ashrrev_i32_e32 v205, 31, v204
	v_cvt_pk_fp8_f32 v88, v80, v81
	s_and_b64 vcc, exec, s[0:1]
	v_cvt_pk_fp8_f32 v88, v82, v83 op_sel:[0,0,1]
	v_lshlrev_b64 v[84:85], 10, v[204:205]
	v_lshl_add_u64 v[86:87], v[122:123], 0, v[84:85]
	global_store_dword v[86:87], v88, off
	v_exp_f32_e32 v72, v72
	v_exp_f32_e32 v73, v73
	v_exp_f32_e32 v74, v74
	v_pk_add_f32 v[72:73], v[72:73], 1.0 op_sel_hi:[1,0]
	v_exp_f32_e32 v75, v75
	v_exp_f32_e32 v76, v76
	v_pk_add_f32 v[74:75], v[74:75], 1.0 op_sel_hi:[1,0]
	v_exp_f32_e32 v77, v77
	v_exp_f32_e32 v78, v78
	v_pk_add_f32 v[76:77], v[76:77], 1.0 op_sel_hi:[1,0]
	v_exp_f32_e32 v79, v79
	v_exp_f32_e32 v68, v68
	v_pk_add_f32 v[78:79], v[78:79], 1.0 op_sel_hi:[1,0]
	v_exp_f32_e32 v69, v69
	v_pk_mul_f32 v[72:73], v[72:73], v[76:77]
	v_exp_f32_e32 v70, v70
	v_pk_mul_f32 v[74:75], v[74:75], v[78:79]
	v_exp_f32_e32 v71, v71
	v_pk_add_f32 v[68:69], v[68:69], 1.0 op_sel_hi:[1,0]
	v_rcp_f32_e32 v72, v72
	v_rcp_f32_e32 v73, v73
	v_pk_add_f32 v[70:71], v[70:71], 1.0 op_sel_hi:[1,0]
	v_rcp_f32_e32 v74, v74
	v_rcp_f32_e32 v75, v75
	v_pk_add_f32 v[76:77], v[76:77], 2.0 op_sel_hi:[1,0] neg_lo:[1,0] neg_hi:[1,0]
	v_rcp_f32_e32 v68, v68
	v_rcp_f32_e32 v69, v69
	v_pk_add_f32 v[78:79], v[78:79], 2.0 op_sel_hi:[1,0] neg_lo:[1,0] neg_hi:[1,0]
	v_rcp_f32_e32 v70, v70
	v_rcp_f32_e32 v71, v71
	v_pk_mul_f32 v[76:77], v[76:77], v[72:73]
	v_pk_mul_f32 v[78:79], v[78:79], v[74:75]
	s_waitcnt lgkmcnt(0)
	v_lshl_add_u64 v[72:73], v[176:177], 0, s[20:21]
	v_pk_fma_f32 v[68:69], v[160:161], v[68:69], v[76:77]
	v_pk_fma_f32 v[70:71], v[162:163], v[70:71], v[78:79]
	global_store_dwordx4 v[72:73], v[68:71], off nt
	s_nop 1
	v_pk_mul_f32 v[68:69], v[68:69], s[96:97] op_sel_hi:[1,0]
	v_pk_mul_f32 v[70:71], v[70:71], s[96:97] op_sel_hi:[1,0]
	v_exp_f32_e32 v64, v64
	v_exp_f32_e32 v65, v65
	v_exp_f32_e32 v66, v66
	v_pk_fma_f32 v[64:65], v[64:65], s[98:99], s[98:99] op_sel_hi:[1,0,0]
	v_exp_f32_e32 v67, v67
	v_exp_f32_e32 v68, v68
	v_pk_fma_f32 v[66:67], v[66:67], s[98:99], s[98:99] op_sel_hi:[1,0,0]
	v_exp_f32_e32 v69, v69
	v_exp_f32_e32 v70, v70
	v_pk_add_f32 v[68:69], v[68:69], 1.0 op_sel_hi:[1,0]
	v_exp_f32_e32 v71, v71
	v_pk_mul_f32 v[64:65], v[64:65], v[68:69]
	v_rcp_f32_e32 v64, v64
	v_pk_add_f32 v[70:71], v[70:71], 1.0 op_sel_hi:[1,0]
	v_rcp_f32_e32 v65, v65
	v_pk_mul_f32 v[66:67], v[66:67], v[70:71]
	v_pk_add_f32 v[68:69], v[68:69], 2.0 op_sel_hi:[1,0] neg_lo:[1,0] neg_hi:[1,0]
	v_rcp_f32_e32 v66, v66
	v_rcp_f32_e32 v67, v67
	v_pk_add_f32 v[70:71], v[70:71], 2.0 op_sel_hi:[1,0] neg_lo:[1,0] neg_hi:[1,0]
	v_pk_mul_f32 v[64:65], v[64:65], v[68:69]
	v_pk_mul_f32 v[66:67], v[66:67], v[70:71]
	v_ashrrev_i32_e32 v203, 31, v202
	v_cvt_pk_fp8_f32 v72, v64, v65
	s_and_b64 vcc, exec, s[0:1]
	v_cvt_pk_fp8_f32 v72, v66, v67 op_sel:[0,0,1]
	v_lshlrev_b64 v[68:69], 10, v[202:203]
	v_lshl_add_u64 v[70:71], v[122:123], 0, v[68:69]
	global_store_dword v[70:71], v72, off
	v_exp_f32_e32 v56, v56
	v_exp_f32_e32 v57, v57
	v_exp_f32_e32 v58, v58
	v_pk_add_f32 v[56:57], v[56:57], 1.0 op_sel_hi:[1,0]
	v_exp_f32_e32 v59, v59
	v_exp_f32_e32 v60, v60
	v_pk_add_f32 v[58:59], v[58:59], 1.0 op_sel_hi:[1,0]
	v_exp_f32_e32 v61, v61
	v_exp_f32_e32 v62, v62
	v_pk_add_f32 v[60:61], v[60:61], 1.0 op_sel_hi:[1,0]
	v_exp_f32_e32 v63, v63
	v_exp_f32_e32 v52, v52
	v_pk_add_f32 v[62:63], v[62:63], 1.0 op_sel_hi:[1,0]
	v_exp_f32_e32 v53, v53
	v_pk_mul_f32 v[56:57], v[56:57], v[60:61]
	v_exp_f32_e32 v54, v54
	v_pk_mul_f32 v[58:59], v[58:59], v[62:63]
	v_exp_f32_e32 v55, v55
	v_pk_add_f32 v[52:53], v[52:53], 1.0 op_sel_hi:[1,0]
	v_rcp_f32_e32 v56, v56
	v_rcp_f32_e32 v57, v57
	v_pk_add_f32 v[54:55], v[54:55], 1.0 op_sel_hi:[1,0]
	v_rcp_f32_e32 v58, v58
	v_rcp_f32_e32 v59, v59
	v_pk_add_f32 v[60:61], v[60:61], 2.0 op_sel_hi:[1,0] neg_lo:[1,0] neg_hi:[1,0]
	v_rcp_f32_e32 v52, v52
	v_rcp_f32_e32 v53, v53
	v_pk_add_f32 v[62:63], v[62:63], 2.0 op_sel_hi:[1,0] neg_lo:[1,0] neg_hi:[1,0]
	v_rcp_f32_e32 v54, v54
	v_rcp_f32_e32 v55, v55
	v_pk_mul_f32 v[60:61], v[60:61], v[56:57]
	v_pk_mul_f32 v[62:63], v[62:63], v[58:59]
	s_waitcnt vmcnt(8)
	v_pk_fma_f32 v[52:53], v[156:157], v[52:53], v[60:61]
	v_pk_fma_f32 v[54:55], v[158:159], v[54:55], v[62:63]
	v_lshl_add_u64 v[56:57], v[176:177], 0, s[14:15]
	global_store_dwordx4 v[56:57], v[52:55], off nt
	s_nop 1
	v_pk_mul_f32 v[52:53], v[52:53], s[96:97] op_sel_hi:[1,0]
	v_pk_mul_f32 v[54:55], v[54:55], s[96:97] op_sel_hi:[1,0]
	v_exp_f32_e32 v48, v48
	v_exp_f32_e32 v49, v49
	v_exp_f32_e32 v50, v50
	v_pk_fma_f32 v[48:49], v[48:49], s[98:99], s[98:99] op_sel_hi:[1,0,0]
	v_exp_f32_e32 v51, v51
	v_exp_f32_e32 v52, v52
	v_pk_fma_f32 v[50:51], v[50:51], s[98:99], s[98:99] op_sel_hi:[1,0,0]
	v_exp_f32_e32 v53, v53
	v_exp_f32_e32 v54, v54
	v_pk_add_f32 v[52:53], v[52:53], 1.0 op_sel_hi:[1,0]
	v_exp_f32_e32 v55, v55
	v_pk_mul_f32 v[48:49], v[48:49], v[52:53]
	v_rcp_f32_e32 v48, v48
	v_pk_add_f32 v[54:55], v[54:55], 1.0 op_sel_hi:[1,0]
	v_rcp_f32_e32 v49, v49
	v_pk_mul_f32 v[50:51], v[50:51], v[54:55]
	v_pk_add_f32 v[52:53], v[52:53], 2.0 op_sel_hi:[1,0] neg_lo:[1,0] neg_hi:[1,0]
	v_rcp_f32_e32 v50, v50
	v_rcp_f32_e32 v51, v51
	v_pk_add_f32 v[54:55], v[54:55], 2.0 op_sel_hi:[1,0] neg_lo:[1,0] neg_hi:[1,0]
	v_pk_mul_f32 v[48:49], v[48:49], v[52:53]
	v_pk_mul_f32 v[50:51], v[50:51], v[54:55]
	v_ashrrev_i32_e32 v201, 31, v200
	v_cvt_pk_fp8_f32 v56, v48, v49
	s_and_b64 vcc, exec, s[0:1]
	v_cvt_pk_fp8_f32 v56, v50, v51 op_sel:[0,0,1]
	v_lshlrev_b64 v[52:53], 10, v[200:201]
	v_lshl_add_u64 v[54:55], v[122:123], 0, v[52:53]
	global_store_dword v[54:55], v56, off
	v_exp_f32_e32 v40, v40
	v_exp_f32_e32 v41, v41
	v_exp_f32_e32 v42, v42
	v_pk_add_f32 v[40:41], v[40:41], 1.0 op_sel_hi:[1,0]
	v_exp_f32_e32 v43, v43
	v_exp_f32_e32 v44, v44
	v_pk_add_f32 v[42:43], v[42:43], 1.0 op_sel_hi:[1,0]
	v_exp_f32_e32 v45, v45
	v_exp_f32_e32 v46, v46
	v_pk_add_f32 v[44:45], v[44:45], 1.0 op_sel_hi:[1,0]
	v_exp_f32_e32 v47, v47
	v_exp_f32_e32 v36, v36
	v_pk_add_f32 v[46:47], v[46:47], 1.0 op_sel_hi:[1,0]
	v_exp_f32_e32 v37, v37
	v_pk_mul_f32 v[40:41], v[40:41], v[44:45]
	v_exp_f32_e32 v38, v38
	v_pk_mul_f32 v[42:43], v[42:43], v[46:47]
	v_exp_f32_e32 v39, v39
	v_pk_add_f32 v[36:37], v[36:37], 1.0 op_sel_hi:[1,0]
	v_rcp_f32_e32 v40, v40
	v_rcp_f32_e32 v41, v41
	v_pk_add_f32 v[38:39], v[38:39], 1.0 op_sel_hi:[1,0]
	v_rcp_f32_e32 v42, v42
	v_rcp_f32_e32 v43, v43
	v_pk_add_f32 v[44:45], v[44:45], 2.0 op_sel_hi:[1,0] neg_lo:[1,0] neg_hi:[1,0]
	v_rcp_f32_e32 v36, v36
	v_rcp_f32_e32 v37, v37
	v_pk_add_f32 v[46:47], v[46:47], 2.0 op_sel_hi:[1,0] neg_lo:[1,0] neg_hi:[1,0]
	v_rcp_f32_e32 v38, v38
	v_rcp_f32_e32 v39, v39
	v_pk_mul_f32 v[44:45], v[44:45], v[40:41]
	v_pk_mul_f32 v[46:47], v[46:47], v[42:43]
	v_lshl_add_u64 v[40:41], v[176:177], 0, s[22:23]
	v_pk_fma_f32 v[36:37], v[152:153], v[36:37], v[44:45]
	v_pk_fma_f32 v[38:39], v[154:155], v[38:39], v[46:47]
	global_store_dwordx4 v[40:41], v[36:39], off nt
	s_nop 1
	v_pk_mul_f32 v[36:37], v[36:37], s[96:97] op_sel_hi:[1,0]
	v_pk_mul_f32 v[38:39], v[38:39], s[96:97] op_sel_hi:[1,0]
	v_exp_f32_e32 v32, v32
	v_exp_f32_e32 v33, v33
	v_exp_f32_e32 v34, v34
	v_pk_fma_f32 v[32:33], v[32:33], s[98:99], s[98:99] op_sel_hi:[1,0,0]
	v_exp_f32_e32 v35, v35
	v_exp_f32_e32 v36, v36
	v_pk_fma_f32 v[34:35], v[34:35], s[98:99], s[98:99] op_sel_hi:[1,0,0]
	v_exp_f32_e32 v37, v37
	v_exp_f32_e32 v38, v38
	v_pk_add_f32 v[36:37], v[36:37], 1.0 op_sel_hi:[1,0]
	v_exp_f32_e32 v39, v39
	v_pk_mul_f32 v[32:33], v[32:33], v[36:37]
	v_rcp_f32_e32 v32, v32
	v_pk_add_f32 v[38:39], v[38:39], 1.0 op_sel_hi:[1,0]
	v_rcp_f32_e32 v33, v33
	v_pk_mul_f32 v[34:35], v[34:35], v[38:39]
	v_pk_add_f32 v[36:37], v[36:37], 2.0 op_sel_hi:[1,0] neg_lo:[1,0] neg_hi:[1,0]
	v_rcp_f32_e32 v34, v34
	v_rcp_f32_e32 v35, v35
	v_pk_add_f32 v[38:39], v[38:39], 2.0 op_sel_hi:[1,0] neg_lo:[1,0] neg_hi:[1,0]
	v_pk_mul_f32 v[32:33], v[32:33], v[36:37]
	v_pk_mul_f32 v[34:35], v[34:35], v[38:39]
	v_cvt_pk_fp8_f32 v40, v32, v33
	v_or_b32_e32 v36, 16, v200
	v_ashrrev_i32_e32 v37, 31, v36
	v_lshlrev_b64 v[36:37], 10, v[36:37]
	v_cvt_pk_fp8_f32 v40, v34, v35 op_sel:[0,0,1]
	v_lshl_add_u64 v[38:39], v[122:123], 0, v[36:37]
	global_store_dword v[38:39], v40, off
	v_exp_f32_e32 v24, v24
	v_exp_f32_e32 v25, v25
	v_exp_f32_e32 v26, v26
	v_pk_add_f32 v[24:25], v[24:25], 1.0 op_sel_hi:[1,0]
	v_exp_f32_e32 v27, v27
	v_exp_f32_e32 v28, v28
	v_pk_add_f32 v[26:27], v[26:27], 1.0 op_sel_hi:[1,0]
	v_exp_f32_e32 v29, v29
	v_exp_f32_e32 v30, v30
	v_pk_add_f32 v[28:29], v[28:29], 1.0 op_sel_hi:[1,0]
	v_exp_f32_e32 v31, v31
	v_exp_f32_e32 v20, v20
	v_pk_add_f32 v[30:31], v[30:31], 1.0 op_sel_hi:[1,0]
	v_exp_f32_e32 v21, v21
	v_pk_mul_f32 v[24:25], v[24:25], v[28:29]
	v_exp_f32_e32 v22, v22
	v_pk_mul_f32 v[26:27], v[26:27], v[30:31]
	v_exp_f32_e32 v23, v23
	v_pk_add_f32 v[20:21], v[20:21], 1.0 op_sel_hi:[1,0]
	v_rcp_f32_e32 v24, v24
	v_rcp_f32_e32 v25, v25
	v_pk_add_f32 v[22:23], v[22:23], 1.0 op_sel_hi:[1,0]
	v_rcp_f32_e32 v26, v26
	v_rcp_f32_e32 v27, v27
	v_pk_add_f32 v[28:29], v[28:29], 2.0 op_sel_hi:[1,0] neg_lo:[1,0] neg_hi:[1,0]
	v_rcp_f32_e32 v20, v20
	v_rcp_f32_e32 v21, v21
	v_pk_add_f32 v[30:31], v[30:31], 2.0 op_sel_hi:[1,0] neg_lo:[1,0] neg_hi:[1,0]
	v_rcp_f32_e32 v22, v22
	v_rcp_f32_e32 v23, v23
	v_pk_mul_f32 v[28:29], v[28:29], v[24:25]
	v_pk_mul_f32 v[30:31], v[30:31], v[26:27]
	v_pk_fma_f32 v[20:21], v[148:149], v[20:21], v[28:29]
	v_pk_fma_f32 v[22:23], v[150:151], v[22:23], v[30:31]
	v_lshl_add_u64 v[24:25], v[176:177], 0, s[16:17]
	global_store_dwordx4 v[24:25], v[20:23], off nt
	s_nop 1
	v_pk_mul_f32 v[20:21], v[20:21], s[96:97] op_sel_hi:[1,0]
	v_pk_mul_f32 v[22:23], v[22:23], s[96:97] op_sel_hi:[1,0]
	v_exp_f32_e32 v16, v16
	v_exp_f32_e32 v17, v17
	v_exp_f32_e32 v18, v18
	v_pk_fma_f32 v[16:17], v[16:17], s[98:99], s[98:99] op_sel_hi:[1,0,0]
	v_exp_f32_e32 v19, v19
	v_exp_f32_e32 v20, v20
	v_pk_fma_f32 v[18:19], v[18:19], s[98:99], s[98:99] op_sel_hi:[1,0,0]
	v_exp_f32_e32 v21, v21
	v_exp_f32_e32 v22, v22
	v_pk_add_f32 v[20:21], v[20:21], 1.0 op_sel_hi:[1,0]
	v_exp_f32_e32 v23, v23
	v_pk_mul_f32 v[16:17], v[16:17], v[20:21]
	v_rcp_f32_e32 v16, v16
	v_pk_add_f32 v[22:23], v[22:23], 1.0 op_sel_hi:[1,0]
	v_rcp_f32_e32 v17, v17
	v_pk_mul_f32 v[18:19], v[18:19], v[22:23]
	v_pk_add_f32 v[20:21], v[20:21], 2.0 op_sel_hi:[1,0] neg_lo:[1,0] neg_hi:[1,0]
	v_rcp_f32_e32 v18, v18
	v_rcp_f32_e32 v19, v19
	v_pk_add_f32 v[22:23], v[22:23], 2.0 op_sel_hi:[1,0] neg_lo:[1,0] neg_hi:[1,0]
	v_pk_mul_f32 v[16:17], v[16:17], v[20:21]
	v_pk_mul_f32 v[18:19], v[18:19], v[22:23]
	v_cvt_pk_fp8_f32 v24, v16, v17
	v_or_b32_e32 v20, 32, v200
	v_ashrrev_i32_e32 v21, 31, v20
	v_lshlrev_b64 v[20:21], 10, v[20:21]
	v_cvt_pk_fp8_f32 v24, v18, v19 op_sel:[0,0,1]
	v_lshl_add_u64 v[22:23], v[122:123], 0, v[20:21]
	global_store_dword v[22:23], v24, off
	v_exp_f32_e32 v8, v8
	v_exp_f32_e32 v9, v9
	v_exp_f32_e32 v10, v10
	v_pk_add_f32 v[8:9], v[8:9], 1.0 op_sel_hi:[1,0]
	v_exp_f32_e32 v11, v11
	v_exp_f32_e32 v12, v12
	v_pk_add_f32 v[10:11], v[10:11], 1.0 op_sel_hi:[1,0]
	v_exp_f32_e32 v13, v13
	v_exp_f32_e32 v14, v14
	v_pk_add_f32 v[12:13], v[12:13], 1.0 op_sel_hi:[1,0]
	v_exp_f32_e32 v15, v15
	v_exp_f32_e32 v4, v4
	v_pk_add_f32 v[14:15], v[14:15], 1.0 op_sel_hi:[1,0]
	v_exp_f32_e32 v5, v5
	v_pk_mul_f32 v[8:9], v[8:9], v[12:13]
	v_exp_f32_e32 v6, v6
	v_pk_mul_f32 v[10:11], v[10:11], v[14:15]
	v_exp_f32_e32 v7, v7
	v_pk_add_f32 v[4:5], v[4:5], 1.0 op_sel_hi:[1,0]
	v_rcp_f32_e32 v8, v8
	v_rcp_f32_e32 v9, v9
	v_pk_add_f32 v[6:7], v[6:7], 1.0 op_sel_hi:[1,0]
	v_rcp_f32_e32 v10, v10
	v_rcp_f32_e32 v11, v11
	v_pk_add_f32 v[12:13], v[12:13], 2.0 op_sel_hi:[1,0] neg_lo:[1,0] neg_hi:[1,0]
	v_rcp_f32_e32 v4, v4
	v_rcp_f32_e32 v5, v5
	v_pk_add_f32 v[14:15], v[14:15], 2.0 op_sel_hi:[1,0] neg_lo:[1,0] neg_hi:[1,0]
	v_rcp_f32_e32 v6, v6
	v_rcp_f32_e32 v7, v7
	v_pk_mul_f32 v[12:13], v[12:13], v[8:9]
	v_pk_mul_f32 v[14:15], v[14:15], v[10:11]
	v_lshl_add_u64 v[8:9], v[176:177], 0, s[24:25]
	v_pk_fma_f32 v[4:5], v[144:145], v[4:5], v[12:13]
	v_pk_fma_f32 v[6:7], v[146:147], v[6:7], v[14:15]
	global_store_dwordx4 v[8:9], v[4:7], off nt
	s_nop 1
	v_pk_mul_f32 v[4:5], v[4:5], s[96:97] op_sel_hi:[1,0]
	v_pk_mul_f32 v[6:7], v[6:7], s[96:97] op_sel_hi:[1,0]
	v_exp_f32_e32 v0, v0
	v_exp_f32_e32 v1, v1
	v_exp_f32_e32 v2, v2
	v_pk_fma_f32 v[0:1], v[0:1], s[98:99], s[98:99] op_sel_hi:[1,0,0]
	v_exp_f32_e32 v3, v3
	v_exp_f32_e32 v4, v4
	v_pk_fma_f32 v[2:3], v[2:3], s[98:99], s[98:99] op_sel_hi:[1,0,0]
	v_exp_f32_e32 v5, v5
	v_exp_f32_e32 v6, v6
	v_pk_add_f32 v[4:5], v[4:5], 1.0 op_sel_hi:[1,0]
	v_exp_f32_e32 v7, v7
	v_pk_mul_f32 v[0:1], v[0:1], v[4:5]
	v_rcp_f32_e32 v0, v0
	v_pk_add_f32 v[6:7], v[6:7], 1.0 op_sel_hi:[1,0]
	v_rcp_f32_e32 v1, v1
	v_pk_mul_f32 v[2:3], v[2:3], v[6:7]
	v_pk_add_f32 v[4:5], v[4:5], 2.0 op_sel_hi:[1,0] neg_lo:[1,0] neg_hi:[1,0]
	v_rcp_f32_e32 v2, v2
	v_rcp_f32_e32 v3, v3
	v_pk_add_f32 v[6:7], v[6:7], 2.0 op_sel_hi:[1,0] neg_lo:[1,0] neg_hi:[1,0]
	v_pk_mul_f32 v[0:1], v[0:1], v[4:5]
	v_pk_mul_f32 v[2:3], v[2:3], v[6:7]
	v_cvt_pk_fp8_f32 v8, v0, v1
	v_or_b32_e32 v4, 48, v200
	v_ashrrev_i32_e32 v5, 31, v4
	v_lshlrev_b64 v[4:5], 10, v[4:5]
	v_cvt_pk_fp8_f32 v8, v2, v3 op_sel:[0,0,1]
	v_lshl_add_u64 v[6:7], v[122:123], 0, v[4:5]
	global_store_dword v[6:7], v8, off
	s_branch .LBB2_24
.Lmy_epi_nl7:
	v_exp_f32_e32 v120, v120
	v_exp_f32_e32 v121, v121
	v_exp_f32_e32 v122, v122
	v_pk_add_f32 v[120:121], v[120:121], 1.0 op_sel_hi:[1,0]
	v_exp_f32_e32 v123, v123
	v_exp_f32_e32 v124, v124
	v_pk_add_f32 v[122:123], v[122:123], 1.0 op_sel_hi:[1,0]
	v_exp_f32_e32 v125, v125
	v_exp_f32_e32 v126, v126
	v_pk_add_f32 v[124:125], v[124:125], 1.0 op_sel_hi:[1,0]
	v_exp_f32_e32 v127, v127
	v_exp_f32_e32 v116, v116
	v_pk_add_f32 v[126:127], v[126:127], 1.0 op_sel_hi:[1,0]
	v_exp_f32_e32 v117, v117
	v_pk_mul_f32 v[120:121], v[120:121], v[124:125]
	v_exp_f32_e32 v118, v118
	v_pk_mul_f32 v[122:123], v[122:123], v[126:127]
	v_exp_f32_e32 v119, v119
	v_pk_add_f32 v[116:117], v[116:117], 1.0 op_sel_hi:[1,0]
	v_rcp_f32_e32 v120, v120
	v_rcp_f32_e32 v121, v121
	v_pk_add_f32 v[118:119], v[118:119], 1.0 op_sel_hi:[1,0]
	v_rcp_f32_e32 v122, v122
	v_rcp_f32_e32 v123, v123
	v_pk_add_f32 v[124:125], v[124:125], 2.0 op_sel_hi:[1,0] neg_lo:[1,0] neg_hi:[1,0]
	v_rcp_f32_e32 v116, v116
	v_rcp_f32_e32 v117, v117
	v_pk_add_f32 v[126:127], v[126:127], 2.0 op_sel_hi:[1,0] neg_lo:[1,0] neg_hi:[1,0]
	v_rcp_f32_e32 v118, v118
	v_rcp_f32_e32 v119, v119
	v_pk_mul_f32 v[124:125], v[124:125], v[120:121]
	v_pk_mul_f32 v[126:127], v[126:127], v[122:123]
	s_waitcnt lgkmcnt(3)
	v_pk_fma_f32 v[116:117], v[172:173], v[116:117], v[124:125]
	v_pk_fma_f32 v[118:119], v[174:175], v[118:119], v[126:127]
	global_store_dwordx4 v[176:177], v[116:119], off nt
	s_nop 1
	v_pk_mul_f32 v[116:117], v[116:117], s[96:97] op_sel_hi:[1,0]
	v_pk_mul_f32 v[118:119], v[118:119], s[96:97] op_sel_hi:[1,0]
	v_exp_f32_e32 v112, v112
	v_exp_f32_e32 v113, v113
	v_exp_f32_e32 v114, v114
	v_pk_fma_f32 v[112:113], v[112:113], s[98:99], s[98:99] op_sel_hi:[1,0,0]
	v_exp_f32_e32 v115, v115
	v_exp_f32_e32 v116, v116
	v_pk_fma_f32 v[114:115], v[114:115], s[98:99], s[98:99] op_sel_hi:[1,0,0]
	v_exp_f32_e32 v117, v117
	v_exp_f32_e32 v118, v118
	v_pk_add_f32 v[116:117], v[116:117], 1.0 op_sel_hi:[1,0]
	v_exp_f32_e32 v119, v119
	v_pk_mul_f32 v[112:113], v[112:113], v[116:117]
	v_rcp_f32_e32 v112, v112
	v_pk_add_f32 v[118:119], v[118:119], 1.0 op_sel_hi:[1,0]
	v_rcp_f32_e32 v113, v113
	v_pk_mul_f32 v[114:115], v[114:115], v[118:119]
	v_pk_add_f32 v[116:117], v[116:117], 2.0 op_sel_hi:[1,0] neg_lo:[1,0] neg_hi:[1,0]
	v_rcp_f32_e32 v114, v114
	v_rcp_f32_e32 v115, v115
	v_pk_add_f32 v[118:119], v[118:119], 2.0 op_sel_hi:[1,0] neg_lo:[1,0] neg_hi:[1,0]
	v_pk_mul_f32 v[112:113], v[112:113], v[116:117]
	v_pk_mul_f32 v[114:115], v[114:115], v[118:119]
	v_cvt_pk_fp8_f32 v124, v112, v113
	s_add_u32 s0, s8, s27
	s_addc_u32 s1, s9, 0
	s_ashr_i32 s35, s34, 31
	s_lshl_b64 s[34:35], s[34:35], 21
	v_ashrrev_i32_e32 v209, 31, v208
	s_add_u32 s36, s73, s34
	v_lshl_add_u64 v[122:123], s[0:1], 0, v[210:211]
	v_cvt_pk_fp8_f32 v124, v114, v115 op_sel:[0,0,1]
	v_lshlrev_b64 v[116:117], 10, v[208:209]
	s_addc_u32 s37, s74, s35
	v_lshl_add_u64 v[118:119], v[122:123], 0, v[116:117]
	global_store_dword v[118:119], v124, off
	s_cmp_eq_u32 s30, 7
	s_cselect_b64 s[34:35], -1, 0
	s_cmp_lg_u32 s30, 7
	v_lshl_add_u64 v[120:121], v[210:211], 1, s[36:37]
	v_pk_mul_f32 v[112:113], v[112:113], s[98:99] op_sel_hi:[1,0]
	v_pk_mul_f32 v[114:115], v[114:115], s[98:99] op_sel_hi:[1,0]
	v_cvt_pk_f16_f32 v112, v112, v113
	v_cvt_pk_f16_f32 v113, v114, v115
	v_lshl_add_u64 v[114:115], v[116:117], 1, v[120:121]
	global_store_dwordx2 v[114:115], v[112:113], off
	v_exp_f32_e32 v104, v104
	v_exp_f32_e32 v105, v105
	v_exp_f32_e32 v106, v106
	v_pk_add_f32 v[104:105], v[104:105], 1.0 op_sel_hi:[1,0]
	v_exp_f32_e32 v107, v107
	v_exp_f32_e32 v108, v108
	v_pk_add_f32 v[106:107], v[106:107], 1.0 op_sel_hi:[1,0]
	v_exp_f32_e32 v109, v109
	v_exp_f32_e32 v110, v110
	v_pk_add_f32 v[108:109], v[108:109], 1.0 op_sel_hi:[1,0]
	v_exp_f32_e32 v111, v111
	v_exp_f32_e32 v100, v100
	v_pk_add_f32 v[110:111], v[110:111], 1.0 op_sel_hi:[1,0]
	v_exp_f32_e32 v101, v101
	v_pk_mul_f32 v[104:105], v[104:105], v[108:109]
	v_exp_f32_e32 v102, v102
	v_pk_mul_f32 v[106:107], v[106:107], v[110:111]
	v_exp_f32_e32 v103, v103
	v_pk_add_f32 v[100:101], v[100:101], 1.0 op_sel_hi:[1,0]
	v_rcp_f32_e32 v104, v104
	v_rcp_f32_e32 v105, v105
	v_pk_add_f32 v[102:103], v[102:103], 1.0 op_sel_hi:[1,0]
	v_rcp_f32_e32 v106, v106
	v_rcp_f32_e32 v107, v107
	v_pk_add_f32 v[108:109], v[108:109], 2.0 op_sel_hi:[1,0] neg_lo:[1,0] neg_hi:[1,0]
	v_rcp_f32_e32 v100, v100
	v_rcp_f32_e32 v101, v101
	v_pk_add_f32 v[110:111], v[110:111], 2.0 op_sel_hi:[1,0] neg_lo:[1,0] neg_hi:[1,0]
	v_rcp_f32_e32 v102, v102
	v_rcp_f32_e32 v103, v103
	v_pk_mul_f32 v[108:109], v[108:109], v[104:105]
	v_pk_mul_f32 v[110:111], v[110:111], v[106:107]
	s_waitcnt lgkmcnt(2)
	v_lshl_add_u64 v[104:105], v[176:177], 0, s[18:19]
	v_pk_fma_f32 v[100:101], v[168:169], v[100:101], v[108:109]
	v_pk_fma_f32 v[102:103], v[170:171], v[102:103], v[110:111]
	global_store_dwordx4 v[104:105], v[100:103], off nt
	s_nop 1
	v_pk_mul_f32 v[100:101], v[100:101], s[96:97] op_sel_hi:[1,0]
	v_pk_mul_f32 v[102:103], v[102:103], s[96:97] op_sel_hi:[1,0]
	v_exp_f32_e32 v96, v96
	v_exp_f32_e32 v97, v97
	v_exp_f32_e32 v98, v98
	v_pk_fma_f32 v[96:97], v[96:97], s[98:99], s[98:99] op_sel_hi:[1,0,0]
	v_exp_f32_e32 v99, v99
	v_exp_f32_e32 v100, v100
	v_pk_fma_f32 v[98:99], v[98:99], s[98:99], s[98:99] op_sel_hi:[1,0,0]
	v_exp_f32_e32 v101, v101
	v_exp_f32_e32 v102, v102
	v_pk_add_f32 v[100:101], v[100:101], 1.0 op_sel_hi:[1,0]
	v_exp_f32_e32 v103, v103
	v_pk_mul_f32 v[96:97], v[96:97], v[100:101]
	v_rcp_f32_e32 v96, v96
	v_pk_add_f32 v[102:103], v[102:103], 1.0 op_sel_hi:[1,0]
	v_rcp_f32_e32 v97, v97
	v_pk_mul_f32 v[98:99], v[98:99], v[102:103]
	v_pk_add_f32 v[100:101], v[100:101], 2.0 op_sel_hi:[1,0] neg_lo:[1,0] neg_hi:[1,0]
	v_rcp_f32_e32 v98, v98
	v_rcp_f32_e32 v99, v99
	v_pk_add_f32 v[102:103], v[102:103], 2.0 op_sel_hi:[1,0] neg_lo:[1,0] neg_hi:[1,0]
	v_pk_mul_f32 v[96:97], v[96:97], v[100:101]
	v_pk_mul_f32 v[98:99], v[98:99], v[102:103]
	v_cvt_pk_fp8_f32 v104, v96, v97
	v_ashrrev_i32_e32 v207, 31, v206
	v_lshlrev_b64 v[100:101], 10, v[206:207]
	v_lshl_add_u64 v[102:103], v[122:123], 0, v[100:101]
	v_cvt_pk_fp8_f32 v104, v98, v99 op_sel:[0,0,1]
	v_cndmask_b32_e64 v105, 0, 1, s[34:35]
	global_store_dword v[102:103], v104, off
	v_cmp_ne_u32_e64 s[0:1], 1, v105
	v_pk_mul_f32 v[96:97], v[96:97], s[98:99] op_sel_hi:[1,0]
	v_pk_mul_f32 v[98:99], v[98:99], s[98:99] op_sel_hi:[1,0]
	v_cvt_pk_f16_f32 v96, v96, v97
	v_cvt_pk_f16_f32 v97, v98, v99
	v_lshl_add_u64 v[98:99], v[100:101], 1, v[120:121]
	global_store_dwordx2 v[98:99], v[96:97], off
	v_exp_f32_e32 v88, v88
	v_exp_f32_e32 v89, v89
	v_exp_f32_e32 v90, v90
	v_pk_add_f32 v[88:89], v[88:89], 1.0 op_sel_hi:[1,0]
	v_exp_f32_e32 v91, v91
	v_exp_f32_e32 v92, v92
	v_pk_add_f32 v[90:91], v[90:91], 1.0 op_sel_hi:[1,0]
	v_exp_f32_e32 v93, v93
	v_exp_f32_e32 v94, v94
	v_pk_add_f32 v[92:93], v[92:93], 1.0 op_sel_hi:[1,0]
	v_exp_f32_e32 v95, v95
	v_exp_f32_e32 v84, v84
	v_pk_add_f32 v[94:95], v[94:95], 1.0 op_sel_hi:[1,0]
	v_exp_f32_e32 v85, v85
	v_pk_mul_f32 v[88:89], v[88:89], v[92:93]
	v_exp_f32_e32 v86, v86
	v_pk_mul_f32 v[90:91], v[90:91], v[94:95]
	v_exp_f32_e32 v87, v87
	v_pk_add_f32 v[84:85], v[84:85], 1.0 op_sel_hi:[1,0]
	v_rcp_f32_e32 v88, v88
	v_rcp_f32_e32 v89, v89
	v_pk_add_f32 v[86:87], v[86:87], 1.0 op_sel_hi:[1,0]
	v_rcp_f32_e32 v90, v90
	v_rcp_f32_e32 v91, v91
	v_pk_add_f32 v[92:93], v[92:93], 2.0 op_sel_hi:[1,0] neg_lo:[1,0] neg_hi:[1,0]
	v_rcp_f32_e32 v84, v84
	v_rcp_f32_e32 v85, v85
	v_pk_add_f32 v[94:95], v[94:95], 2.0 op_sel_hi:[1,0] neg_lo:[1,0] neg_hi:[1,0]
	v_rcp_f32_e32 v86, v86
	v_rcp_f32_e32 v87, v87
	v_pk_mul_f32 v[92:93], v[92:93], v[88:89]
	v_pk_mul_f32 v[94:95], v[94:95], v[90:91]
	s_waitcnt lgkmcnt(1)
	v_pk_fma_f32 v[84:85], v[164:165], v[84:85], v[92:93]
	v_pk_fma_f32 v[86:87], v[166:167], v[86:87], v[94:95]
	v_lshl_add_u64 v[88:89], v[176:177], 0, s[12:13]
	global_store_dwordx4 v[88:89], v[84:87], off nt
	s_nop 1
	v_pk_mul_f32 v[84:85], v[84:85], s[96:97] op_sel_hi:[1,0]
	v_pk_mul_f32 v[86:87], v[86:87], s[96:97] op_sel_hi:[1,0]
	v_exp_f32_e32 v80, v80
	v_exp_f32_e32 v81, v81
	v_exp_f32_e32 v82, v82
	v_pk_fma_f32 v[80:81], v[80:81], s[98:99], s[98:99] op_sel_hi:[1,0,0]
	v_exp_f32_e32 v83, v83
	v_exp_f32_e32 v84, v84
	v_pk_fma_f32 v[82:83], v[82:83], s[98:99], s[98:99] op_sel_hi:[1,0,0]
	v_exp_f32_e32 v85, v85
	v_exp_f32_e32 v86, v86
	v_pk_add_f32 v[84:85], v[84:85], 1.0 op_sel_hi:[1,0]
	v_exp_f32_e32 v87, v87
	v_pk_mul_f32 v[80:81], v[80:81], v[84:85]
	v_rcp_f32_e32 v80, v80
	v_pk_add_f32 v[86:87], v[86:87], 1.0 op_sel_hi:[1,0]
	v_rcp_f32_e32 v81, v81
	v_pk_mul_f32 v[82:83], v[82:83], v[86:87]
	v_pk_add_f32 v[84:85], v[84:85], 2.0 op_sel_hi:[1,0] neg_lo:[1,0] neg_hi:[1,0]
	v_rcp_f32_e32 v82, v82
	v_rcp_f32_e32 v83, v83
	v_pk_add_f32 v[86:87], v[86:87], 2.0 op_sel_hi:[1,0] neg_lo:[1,0] neg_hi:[1,0]
	v_pk_mul_f32 v[80:81], v[80:81], v[84:85]
	v_pk_mul_f32 v[82:83], v[82:83], v[86:87]
	v_ashrrev_i32_e32 v205, 31, v204
	v_cvt_pk_fp8_f32 v88, v80, v81
	s_and_b64 vcc, exec, s[0:1]
	v_cvt_pk_fp8_f32 v88, v82, v83 op_sel:[0,0,1]
	v_lshlrev_b64 v[84:85], 10, v[204:205]
	v_lshl_add_u64 v[86:87], v[122:123], 0, v[84:85]
	global_store_dword v[86:87], v88, off
	v_pk_mul_f32 v[80:81], v[80:81], s[98:99] op_sel_hi:[1,0]
	v_pk_mul_f32 v[82:83], v[82:83], s[98:99] op_sel_hi:[1,0]
	v_cvt_pk_f16_f32 v80, v80, v81
	v_cvt_pk_f16_f32 v81, v82, v83
	v_lshl_add_u64 v[82:83], v[84:85], 1, v[120:121]
	global_store_dwordx2 v[82:83], v[80:81], off
	v_exp_f32_e32 v72, v72
	v_exp_f32_e32 v73, v73
	v_exp_f32_e32 v74, v74
	v_pk_add_f32 v[72:73], v[72:73], 1.0 op_sel_hi:[1,0]
	v_exp_f32_e32 v75, v75
	v_exp_f32_e32 v76, v76
	v_pk_add_f32 v[74:75], v[74:75], 1.0 op_sel_hi:[1,0]
	v_exp_f32_e32 v77, v77
	v_exp_f32_e32 v78, v78
	v_pk_add_f32 v[76:77], v[76:77], 1.0 op_sel_hi:[1,0]
	v_exp_f32_e32 v79, v79
	v_exp_f32_e32 v68, v68
	v_pk_add_f32 v[78:79], v[78:79], 1.0 op_sel_hi:[1,0]
	v_exp_f32_e32 v69, v69
	v_pk_mul_f32 v[72:73], v[72:73], v[76:77]
	v_exp_f32_e32 v70, v70
	v_pk_mul_f32 v[74:75], v[74:75], v[78:79]
	v_exp_f32_e32 v71, v71
	v_pk_add_f32 v[68:69], v[68:69], 1.0 op_sel_hi:[1,0]
	v_rcp_f32_e32 v72, v72
	v_rcp_f32_e32 v73, v73
	v_pk_add_f32 v[70:71], v[70:71], 1.0 op_sel_hi:[1,0]
	v_rcp_f32_e32 v74, v74
	v_rcp_f32_e32 v75, v75
	v_pk_add_f32 v[76:77], v[76:77], 2.0 op_sel_hi:[1,0] neg_lo:[1,0] neg_hi:[1,0]
	v_rcp_f32_e32 v68, v68
	v_rcp_f32_e32 v69, v69
	v_pk_add_f32 v[78:79], v[78:79], 2.0 op_sel_hi:[1,0] neg_lo:[1,0] neg_hi:[1,0]
	v_rcp_f32_e32 v70, v70
	v_rcp_f32_e32 v71, v71
	v_pk_mul_f32 v[76:77], v[76:77], v[72:73]
	v_pk_mul_f32 v[78:79], v[78:79], v[74:75]
	s_waitcnt lgkmcnt(0)
	v_lshl_add_u64 v[72:73], v[176:177], 0, s[20:21]
	v_pk_fma_f32 v[68:69], v[160:161], v[68:69], v[76:77]
	v_pk_fma_f32 v[70:71], v[162:163], v[70:71], v[78:79]
	global_store_dwordx4 v[72:73], v[68:71], off nt
	s_nop 1
	v_pk_mul_f32 v[68:69], v[68:69], s[96:97] op_sel_hi:[1,0]
	v_pk_mul_f32 v[70:71], v[70:71], s[96:97] op_sel_hi:[1,0]
	v_exp_f32_e32 v64, v64
	v_exp_f32_e32 v65, v65
	v_exp_f32_e32 v66, v66
	v_pk_fma_f32 v[64:65], v[64:65], s[98:99], s[98:99] op_sel_hi:[1,0,0]
	v_exp_f32_e32 v67, v67
	v_exp_f32_e32 v68, v68
	v_pk_fma_f32 v[66:67], v[66:67], s[98:99], s[98:99] op_sel_hi:[1,0,0]
	v_exp_f32_e32 v69, v69
	v_exp_f32_e32 v70, v70
	v_pk_add_f32 v[68:69], v[68:69], 1.0 op_sel_hi:[1,0]
	v_exp_f32_e32 v71, v71
	v_pk_mul_f32 v[64:65], v[64:65], v[68:69]
	v_rcp_f32_e32 v64, v64
	v_pk_add_f32 v[70:71], v[70:71], 1.0 op_sel_hi:[1,0]
	v_rcp_f32_e32 v65, v65
	v_pk_mul_f32 v[66:67], v[66:67], v[70:71]
	v_pk_add_f32 v[68:69], v[68:69], 2.0 op_sel_hi:[1,0] neg_lo:[1,0] neg_hi:[1,0]
	v_rcp_f32_e32 v66, v66
	v_rcp_f32_e32 v67, v67
	v_pk_add_f32 v[70:71], v[70:71], 2.0 op_sel_hi:[1,0] neg_lo:[1,0] neg_hi:[1,0]
	v_pk_mul_f32 v[64:65], v[64:65], v[68:69]
	v_pk_mul_f32 v[66:67], v[66:67], v[70:71]
	v_ashrrev_i32_e32 v203, 31, v202
	v_cvt_pk_fp8_f32 v72, v64, v65
	s_and_b64 vcc, exec, s[0:1]
	v_cvt_pk_fp8_f32 v72, v66, v67 op_sel:[0,0,1]
	v_lshlrev_b64 v[68:69], 10, v[202:203]
	v_lshl_add_u64 v[70:71], v[122:123], 0, v[68:69]
	global_store_dword v[70:71], v72, off
	v_pk_mul_f32 v[64:65], v[64:65], s[98:99] op_sel_hi:[1,0]
	v_pk_mul_f32 v[66:67], v[66:67], s[98:99] op_sel_hi:[1,0]
	v_cvt_pk_f16_f32 v64, v64, v65
	v_cvt_pk_f16_f32 v65, v66, v67
	v_lshl_add_u64 v[66:67], v[68:69], 1, v[120:121]
	global_store_dwordx2 v[66:67], v[64:65], off
	v_exp_f32_e32 v56, v56
	v_exp_f32_e32 v57, v57
	v_exp_f32_e32 v58, v58
	v_pk_add_f32 v[56:57], v[56:57], 1.0 op_sel_hi:[1,0]
	v_exp_f32_e32 v59, v59
	v_exp_f32_e32 v60, v60
	v_pk_add_f32 v[58:59], v[58:59], 1.0 op_sel_hi:[1,0]
	v_exp_f32_e32 v61, v61
	v_exp_f32_e32 v62, v62
	v_pk_add_f32 v[60:61], v[60:61], 1.0 op_sel_hi:[1,0]
	v_exp_f32_e32 v63, v63
	v_exp_f32_e32 v52, v52
	v_pk_add_f32 v[62:63], v[62:63], 1.0 op_sel_hi:[1,0]
	v_exp_f32_e32 v53, v53
	v_pk_mul_f32 v[56:57], v[56:57], v[60:61]
	v_exp_f32_e32 v54, v54
	v_pk_mul_f32 v[58:59], v[58:59], v[62:63]
	v_exp_f32_e32 v55, v55
	v_pk_add_f32 v[52:53], v[52:53], 1.0 op_sel_hi:[1,0]
	v_rcp_f32_e32 v56, v56
	v_rcp_f32_e32 v57, v57
	v_pk_add_f32 v[54:55], v[54:55], 1.0 op_sel_hi:[1,0]
	v_rcp_f32_e32 v58, v58
	v_rcp_f32_e32 v59, v59
	v_pk_add_f32 v[60:61], v[60:61], 2.0 op_sel_hi:[1,0] neg_lo:[1,0] neg_hi:[1,0]
	v_rcp_f32_e32 v52, v52
	v_rcp_f32_e32 v53, v53
	v_pk_add_f32 v[62:63], v[62:63], 2.0 op_sel_hi:[1,0] neg_lo:[1,0] neg_hi:[1,0]
	v_rcp_f32_e32 v54, v54
	v_rcp_f32_e32 v55, v55
	v_pk_mul_f32 v[60:61], v[60:61], v[56:57]
	v_pk_mul_f32 v[62:63], v[62:63], v[58:59]
	s_waitcnt vmcnt(8)
	v_pk_fma_f32 v[52:53], v[156:157], v[52:53], v[60:61]
	v_pk_fma_f32 v[54:55], v[158:159], v[54:55], v[62:63]
	v_lshl_add_u64 v[56:57], v[176:177], 0, s[14:15]
	global_store_dwordx4 v[56:57], v[52:55], off nt
	s_nop 1
	v_pk_mul_f32 v[52:53], v[52:53], s[96:97] op_sel_hi:[1,0]
	v_pk_mul_f32 v[54:55], v[54:55], s[96:97] op_sel_hi:[1,0]
	v_exp_f32_e32 v48, v48
	v_exp_f32_e32 v49, v49
	v_exp_f32_e32 v50, v50
	v_pk_fma_f32 v[48:49], v[48:49], s[98:99], s[98:99] op_sel_hi:[1,0,0]
	v_exp_f32_e32 v51, v51
	v_exp_f32_e32 v52, v52
	v_pk_fma_f32 v[50:51], v[50:51], s[98:99], s[98:99] op_sel_hi:[1,0,0]
	v_exp_f32_e32 v53, v53
	v_exp_f32_e32 v54, v54
	v_pk_add_f32 v[52:53], v[52:53], 1.0 op_sel_hi:[1,0]
	v_exp_f32_e32 v55, v55
	v_pk_mul_f32 v[48:49], v[48:49], v[52:53]
	v_rcp_f32_e32 v48, v48
	v_pk_add_f32 v[54:55], v[54:55], 1.0 op_sel_hi:[1,0]
	v_rcp_f32_e32 v49, v49
	v_pk_mul_f32 v[50:51], v[50:51], v[54:55]
	v_pk_add_f32 v[52:53], v[52:53], 2.0 op_sel_hi:[1,0] neg_lo:[1,0] neg_hi:[1,0]
	v_rcp_f32_e32 v50, v50
	v_rcp_f32_e32 v51, v51
	v_pk_add_f32 v[54:55], v[54:55], 2.0 op_sel_hi:[1,0] neg_lo:[1,0] neg_hi:[1,0]
	v_pk_mul_f32 v[48:49], v[48:49], v[52:53]
	v_pk_mul_f32 v[50:51], v[50:51], v[54:55]
	v_ashrrev_i32_e32 v201, 31, v200
	v_cvt_pk_fp8_f32 v56, v48, v49
	s_and_b64 vcc, exec, s[0:1]
	v_cvt_pk_fp8_f32 v56, v50, v51 op_sel:[0,0,1]
	v_lshlrev_b64 v[52:53], 10, v[200:201]
	v_lshl_add_u64 v[54:55], v[122:123], 0, v[52:53]
	global_store_dword v[54:55], v56, off
	v_pk_mul_f32 v[48:49], v[48:49], s[98:99] op_sel_hi:[1,0]
	v_pk_mul_f32 v[50:51], v[50:51], s[98:99] op_sel_hi:[1,0]
	v_cvt_pk_f16_f32 v48, v48, v49
	v_cvt_pk_f16_f32 v49, v50, v51
	v_lshl_add_u64 v[50:51], v[52:53], 1, v[120:121]
	global_store_dwordx2 v[50:51], v[48:49], off
	v_exp_f32_e32 v40, v40
	v_exp_f32_e32 v41, v41
	v_exp_f32_e32 v42, v42
	v_pk_add_f32 v[40:41], v[40:41], 1.0 op_sel_hi:[1,0]
	v_exp_f32_e32 v43, v43
	v_exp_f32_e32 v44, v44
	v_pk_add_f32 v[42:43], v[42:43], 1.0 op_sel_hi:[1,0]
	v_exp_f32_e32 v45, v45
	v_exp_f32_e32 v46, v46
	v_pk_add_f32 v[44:45], v[44:45], 1.0 op_sel_hi:[1,0]
	v_exp_f32_e32 v47, v47
	v_exp_f32_e32 v36, v36
	v_pk_add_f32 v[46:47], v[46:47], 1.0 op_sel_hi:[1,0]
	v_exp_f32_e32 v37, v37
	v_pk_mul_f32 v[40:41], v[40:41], v[44:45]
	v_exp_f32_e32 v38, v38
	v_pk_mul_f32 v[42:43], v[42:43], v[46:47]
	v_exp_f32_e32 v39, v39
	v_pk_add_f32 v[36:37], v[36:37], 1.0 op_sel_hi:[1,0]
	v_rcp_f32_e32 v40, v40
	v_rcp_f32_e32 v41, v41
	v_pk_add_f32 v[38:39], v[38:39], 1.0 op_sel_hi:[1,0]
	v_rcp_f32_e32 v42, v42
	v_rcp_f32_e32 v43, v43
	v_pk_add_f32 v[44:45], v[44:45], 2.0 op_sel_hi:[1,0] neg_lo:[1,0] neg_hi:[1,0]
	v_rcp_f32_e32 v36, v36
	v_rcp_f32_e32 v37, v37
	v_pk_add_f32 v[46:47], v[46:47], 2.0 op_sel_hi:[1,0] neg_lo:[1,0] neg_hi:[1,0]
	v_rcp_f32_e32 v38, v38
	v_rcp_f32_e32 v39, v39
	v_pk_mul_f32 v[44:45], v[44:45], v[40:41]
	v_pk_mul_f32 v[46:47], v[46:47], v[42:43]
	v_lshl_add_u64 v[40:41], v[176:177], 0, s[22:23]
	v_pk_fma_f32 v[36:37], v[152:153], v[36:37], v[44:45]
	v_pk_fma_f32 v[38:39], v[154:155], v[38:39], v[46:47]
	global_store_dwordx4 v[40:41], v[36:39], off nt
	s_nop 1
	v_pk_mul_f32 v[36:37], v[36:37], s[96:97] op_sel_hi:[1,0]
	v_pk_mul_f32 v[38:39], v[38:39], s[96:97] op_sel_hi:[1,0]
	v_exp_f32_e32 v32, v32
	v_exp_f32_e32 v33, v33
	v_exp_f32_e32 v34, v34
	v_pk_fma_f32 v[32:33], v[32:33], s[98:99], s[98:99] op_sel_hi:[1,0,0]
	v_exp_f32_e32 v35, v35
	v_exp_f32_e32 v36, v36
	v_pk_fma_f32 v[34:35], v[34:35], s[98:99], s[98:99] op_sel_hi:[1,0,0]
	v_exp_f32_e32 v37, v37
	v_exp_f32_e32 v38, v38
	v_pk_add_f32 v[36:37], v[36:37], 1.0 op_sel_hi:[1,0]
	v_exp_f32_e32 v39, v39
	v_pk_mul_f32 v[32:33], v[32:33], v[36:37]
	v_rcp_f32_e32 v32, v32
	v_pk_add_f32 v[38:39], v[38:39], 1.0 op_sel_hi:[1,0]
	v_rcp_f32_e32 v33, v33
	v_pk_mul_f32 v[34:35], v[34:35], v[38:39]
	v_pk_add_f32 v[36:37], v[36:37], 2.0 op_sel_hi:[1,0] neg_lo:[1,0] neg_hi:[1,0]
	v_rcp_f32_e32 v34, v34
	v_rcp_f32_e32 v35, v35
	v_pk_add_f32 v[38:39], v[38:39], 2.0 op_sel_hi:[1,0] neg_lo:[1,0] neg_hi:[1,0]
	v_pk_mul_f32 v[32:33], v[32:33], v[36:37]
	v_pk_mul_f32 v[34:35], v[34:35], v[38:39]
	v_cvt_pk_fp8_f32 v40, v32, v33
	v_or_b32_e32 v36, 16, v200
	v_ashrrev_i32_e32 v37, 31, v36
	v_lshlrev_b64 v[36:37], 10, v[36:37]
	v_cvt_pk_fp8_f32 v40, v34, v35 op_sel:[0,0,1]
	v_lshl_add_u64 v[38:39], v[122:123], 0, v[36:37]
	global_store_dword v[38:39], v40, off
	v_pk_mul_f32 v[32:33], v[32:33], s[98:99] op_sel_hi:[1,0]
	v_pk_mul_f32 v[34:35], v[34:35], s[98:99] op_sel_hi:[1,0]
	v_cvt_pk_f16_f32 v32, v32, v33
	v_cvt_pk_f16_f32 v33, v34, v35
	v_lshl_add_u64 v[34:35], v[36:37], 1, v[120:121]
	global_store_dwordx2 v[34:35], v[32:33], off
	v_exp_f32_e32 v24, v24
	v_exp_f32_e32 v25, v25
	v_exp_f32_e32 v26, v26
	v_pk_add_f32 v[24:25], v[24:25], 1.0 op_sel_hi:[1,0]
	v_exp_f32_e32 v27, v27
	v_exp_f32_e32 v28, v28
	v_pk_add_f32 v[26:27], v[26:27], 1.0 op_sel_hi:[1,0]
	v_exp_f32_e32 v29, v29
	v_exp_f32_e32 v30, v30
	v_pk_add_f32 v[28:29], v[28:29], 1.0 op_sel_hi:[1,0]
	v_exp_f32_e32 v31, v31
	v_exp_f32_e32 v20, v20
	v_pk_add_f32 v[30:31], v[30:31], 1.0 op_sel_hi:[1,0]
	v_exp_f32_e32 v21, v21
	v_pk_mul_f32 v[24:25], v[24:25], v[28:29]
	v_exp_f32_e32 v22, v22
	v_pk_mul_f32 v[26:27], v[26:27], v[30:31]
	v_exp_f32_e32 v23, v23
	v_pk_add_f32 v[20:21], v[20:21], 1.0 op_sel_hi:[1,0]
	v_rcp_f32_e32 v24, v24
	v_rcp_f32_e32 v25, v25
	v_pk_add_f32 v[22:23], v[22:23], 1.0 op_sel_hi:[1,0]
	v_rcp_f32_e32 v26, v26
	v_rcp_f32_e32 v27, v27
	v_pk_add_f32 v[28:29], v[28:29], 2.0 op_sel_hi:[1,0] neg_lo:[1,0] neg_hi:[1,0]
	v_rcp_f32_e32 v20, v20
	v_rcp_f32_e32 v21, v21
	v_pk_add_f32 v[30:31], v[30:31], 2.0 op_sel_hi:[1,0] neg_lo:[1,0] neg_hi:[1,0]
	v_rcp_f32_e32 v22, v22
	v_rcp_f32_e32 v23, v23
	v_pk_mul_f32 v[28:29], v[28:29], v[24:25]
	v_pk_mul_f32 v[30:31], v[30:31], v[26:27]
	v_pk_fma_f32 v[20:21], v[148:149], v[20:21], v[28:29]
	v_pk_fma_f32 v[22:23], v[150:151], v[22:23], v[30:31]
	v_lshl_add_u64 v[24:25], v[176:177], 0, s[16:17]
	global_store_dwordx4 v[24:25], v[20:23], off nt
	s_nop 1
	v_pk_mul_f32 v[20:21], v[20:21], s[96:97] op_sel_hi:[1,0]
	v_pk_mul_f32 v[22:23], v[22:23], s[96:97] op_sel_hi:[1,0]
	v_exp_f32_e32 v16, v16
	v_exp_f32_e32 v17, v17
	v_exp_f32_e32 v18, v18
	v_pk_fma_f32 v[16:17], v[16:17], s[98:99], s[98:99] op_sel_hi:[1,0,0]
	v_exp_f32_e32 v19, v19
	v_exp_f32_e32 v20, v20
	v_pk_fma_f32 v[18:19], v[18:19], s[98:99], s[98:99] op_sel_hi:[1,0,0]
	v_exp_f32_e32 v21, v21
	v_exp_f32_e32 v22, v22
	v_pk_add_f32 v[20:21], v[20:21], 1.0 op_sel_hi:[1,0]
	v_exp_f32_e32 v23, v23
	v_pk_mul_f32 v[16:17], v[16:17], v[20:21]
	v_rcp_f32_e32 v16, v16
	v_pk_add_f32 v[22:23], v[22:23], 1.0 op_sel_hi:[1,0]
	v_rcp_f32_e32 v17, v17
	v_pk_mul_f32 v[18:19], v[18:19], v[22:23]
	v_pk_add_f32 v[20:21], v[20:21], 2.0 op_sel_hi:[1,0] neg_lo:[1,0] neg_hi:[1,0]
	v_rcp_f32_e32 v18, v18
	v_rcp_f32_e32 v19, v19
	v_pk_add_f32 v[22:23], v[22:23], 2.0 op_sel_hi:[1,0] neg_lo:[1,0] neg_hi:[1,0]
	v_pk_mul_f32 v[16:17], v[16:17], v[20:21]
	v_pk_mul_f32 v[18:19], v[18:19], v[22:23]
	v_cvt_pk_fp8_f32 v24, v16, v17
	v_or_b32_e32 v20, 32, v200
	v_ashrrev_i32_e32 v21, 31, v20
	v_lshlrev_b64 v[20:21], 10, v[20:21]
	v_cvt_pk_fp8_f32 v24, v18, v19 op_sel:[0,0,1]
	v_lshl_add_u64 v[22:23], v[122:123], 0, v[20:21]
	global_store_dword v[22:23], v24, off
	v_pk_mul_f32 v[16:17], v[16:17], s[98:99] op_sel_hi:[1,0]
	v_pk_mul_f32 v[18:19], v[18:19], s[98:99] op_sel_hi:[1,0]
	v_cvt_pk_f16_f32 v16, v16, v17
	v_cvt_pk_f16_f32 v17, v18, v19
	v_lshl_add_u64 v[18:19], v[20:21], 1, v[120:121]
	global_store_dwordx2 v[18:19], v[16:17], off
	v_exp_f32_e32 v8, v8
	v_exp_f32_e32 v9, v9
	v_exp_f32_e32 v10, v10
	v_pk_add_f32 v[8:9], v[8:9], 1.0 op_sel_hi:[1,0]
	v_exp_f32_e32 v11, v11
	v_exp_f32_e32 v12, v12
	v_pk_add_f32 v[10:11], v[10:11], 1.0 op_sel_hi:[1,0]
	v_exp_f32_e32 v13, v13
	v_exp_f32_e32 v14, v14
	v_pk_add_f32 v[12:13], v[12:13], 1.0 op_sel_hi:[1,0]
	v_exp_f32_e32 v15, v15
	v_exp_f32_e32 v4, v4
	v_pk_add_f32 v[14:15], v[14:15], 1.0 op_sel_hi:[1,0]
	v_exp_f32_e32 v5, v5
	v_pk_mul_f32 v[8:9], v[8:9], v[12:13]
	v_exp_f32_e32 v6, v6
	v_pk_mul_f32 v[10:11], v[10:11], v[14:15]
	v_exp_f32_e32 v7, v7
	v_pk_add_f32 v[4:5], v[4:5], 1.0 op_sel_hi:[1,0]
	v_rcp_f32_e32 v8, v8
	v_rcp_f32_e32 v9, v9
	v_pk_add_f32 v[6:7], v[6:7], 1.0 op_sel_hi:[1,0]
	v_rcp_f32_e32 v10, v10
	v_rcp_f32_e32 v11, v11
	v_pk_add_f32 v[12:13], v[12:13], 2.0 op_sel_hi:[1,0] neg_lo:[1,0] neg_hi:[1,0]
	v_rcp_f32_e32 v4, v4
	v_rcp_f32_e32 v5, v5
	v_pk_add_f32 v[14:15], v[14:15], 2.0 op_sel_hi:[1,0] neg_lo:[1,0] neg_hi:[1,0]
	v_rcp_f32_e32 v6, v6
	v_rcp_f32_e32 v7, v7
	v_pk_mul_f32 v[12:13], v[12:13], v[8:9]
	v_pk_mul_f32 v[14:15], v[14:15], v[10:11]
	v_lshl_add_u64 v[8:9], v[176:177], 0, s[24:25]
	v_pk_fma_f32 v[4:5], v[144:145], v[4:5], v[12:13]
	v_pk_fma_f32 v[6:7], v[146:147], v[6:7], v[14:15]
	global_store_dwordx4 v[8:9], v[4:7], off nt
	s_nop 1
	v_pk_mul_f32 v[4:5], v[4:5], s[96:97] op_sel_hi:[1,0]
	v_pk_mul_f32 v[6:7], v[6:7], s[96:97] op_sel_hi:[1,0]
	v_exp_f32_e32 v0, v0
	v_exp_f32_e32 v1, v1
	v_exp_f32_e32 v2, v2
	v_pk_fma_f32 v[0:1], v[0:1], s[98:99], s[98:99] op_sel_hi:[1,0,0]
	v_exp_f32_e32 v3, v3
	v_exp_f32_e32 v4, v4
	v_pk_fma_f32 v[2:3], v[2:3], s[98:99], s[98:99] op_sel_hi:[1,0,0]
	v_exp_f32_e32 v5, v5
	v_exp_f32_e32 v6, v6
	v_pk_add_f32 v[4:5], v[4:5], 1.0 op_sel_hi:[1,0]
	v_exp_f32_e32 v7, v7
	v_pk_mul_f32 v[0:1], v[0:1], v[4:5]
	v_rcp_f32_e32 v0, v0
	v_pk_add_f32 v[6:7], v[6:7], 1.0 op_sel_hi:[1,0]
	v_rcp_f32_e32 v1, v1
	v_pk_mul_f32 v[2:3], v[2:3], v[6:7]
	v_pk_add_f32 v[4:5], v[4:5], 2.0 op_sel_hi:[1,0] neg_lo:[1,0] neg_hi:[1,0]
	v_rcp_f32_e32 v2, v2
	v_rcp_f32_e32 v3, v3
	v_pk_add_f32 v[6:7], v[6:7], 2.0 op_sel_hi:[1,0] neg_lo:[1,0] neg_hi:[1,0]
	v_pk_mul_f32 v[0:1], v[0:1], v[4:5]
	v_pk_mul_f32 v[2:3], v[2:3], v[6:7]
	v_cvt_pk_fp8_f32 v8, v0, v1
	v_or_b32_e32 v4, 48, v200
	v_ashrrev_i32_e32 v5, 31, v4
	v_lshlrev_b64 v[4:5], 10, v[4:5]
	v_cvt_pk_fp8_f32 v8, v2, v3 op_sel:[0,0,1]
	v_lshl_add_u64 v[6:7], v[122:123], 0, v[4:5]
	global_store_dword v[6:7], v8, off
	v_pk_mul_f32 v[0:1], v[0:1], s[98:99] op_sel_hi:[1,0]
	v_pk_mul_f32 v[2:3], v[2:3], s[98:99] op_sel_hi:[1,0]
	v_cvt_pk_f16_f32 v0, v0, v1
	v_cvt_pk_f16_f32 v1, v2, v3
	v_lshl_add_u64 v[2:3], v[4:5], 1, v[120:121]
	global_store_dwordx2 v[2:3], v[0:1], off
	s_branch .LBB2_24
.Lmy_epi_last:
	s_cmp_eq_u32 s30, 7
	s_cbranch_scc1 .Lmy_epi_l7
	v_exp_f32_e32 v120, v120
	v_exp_f32_e32 v121, v121
	v_exp_f32_e32 v122, v122
	v_pk_add_f32 v[120:121], v[120:121], 1.0 op_sel_hi:[1,0]
	v_exp_f32_e32 v123, v123
	v_exp_f32_e32 v124, v124
	v_pk_add_f32 v[122:123], v[122:123], 1.0 op_sel_hi:[1,0]
	v_exp_f32_e32 v125, v125
	v_exp_f32_e32 v126, v126
	v_pk_add_f32 v[124:125], v[124:125], 1.0 op_sel_hi:[1,0]
	v_exp_f32_e32 v127, v127
	v_exp_f32_e32 v116, v116
	v_pk_add_f32 v[126:127], v[126:127], 1.0 op_sel_hi:[1,0]
	v_exp_f32_e32 v117, v117
	v_pk_mul_f32 v[120:121], v[120:121], v[124:125]
	v_exp_f32_e32 v118, v118
	v_pk_mul_f32 v[122:123], v[122:123], v[126:127]
	v_exp_f32_e32 v119, v119
	v_pk_add_f32 v[116:117], v[116:117], 1.0 op_sel_hi:[1,0]
	v_rcp_f32_e32 v120, v120
	v_rcp_f32_e32 v121, v121
	v_pk_add_f32 v[118:119], v[118:119], 1.0 op_sel_hi:[1,0]
	v_rcp_f32_e32 v122, v122
	v_rcp_f32_e32 v123, v123
	v_pk_add_f32 v[124:125], v[124:125], 2.0 op_sel_hi:[1,0] neg_lo:[1,0] neg_hi:[1,0]
	v_rcp_f32_e32 v116, v116
	v_rcp_f32_e32 v117, v117
	v_pk_add_f32 v[126:127], v[126:127], 2.0 op_sel_hi:[1,0] neg_lo:[1,0] neg_hi:[1,0]
	v_rcp_f32_e32 v118, v118
	v_rcp_f32_e32 v119, v119
	v_pk_mul_f32 v[124:125], v[124:125], v[120:121]
	v_pk_mul_f32 v[126:127], v[126:127], v[122:123]
	s_waitcnt lgkmcnt(3)
	v_pk_fma_f32 v[116:117], v[172:173], v[116:117], v[124:125]
	v_pk_fma_f32 v[118:119], v[174:175], v[118:119], v[126:127]
	global_store_dwordx4 v[176:177], v[116:119], off sc1
	s_nop 1
	v_pk_mul_f32 v[116:117], v[116:117], s[96:97] op_sel_hi:[1,0]
	v_pk_mul_f32 v[118:119], v[118:119], s[96:97] op_sel_hi:[1,0]
	v_exp_f32_e32 v112, v112
	v_exp_f32_e32 v113, v113
	v_exp_f32_e32 v114, v114
	v_pk_fma_f32 v[112:113], v[112:113], s[98:99], s[98:99] op_sel_hi:[1,0,0]
	v_exp_f32_e32 v115, v115
	v_exp_f32_e32 v116, v116
	v_pk_fma_f32 v[114:115], v[114:115], s[98:99], s[98:99] op_sel_hi:[1,0,0]
	v_exp_f32_e32 v117, v117
	v_exp_f32_e32 v118, v118
	v_pk_add_f32 v[116:117], v[116:117], 1.0 op_sel_hi:[1,0]
	v_exp_f32_e32 v119, v119
	v_pk_mul_f32 v[112:113], v[112:113], v[116:117]
	v_rcp_f32_e32 v112, v112
	v_pk_add_f32 v[118:119], v[118:119], 1.0 op_sel_hi:[1,0]
	v_rcp_f32_e32 v113, v113
	v_pk_mul_f32 v[114:115], v[114:115], v[118:119]
	v_pk_add_f32 v[116:117], v[116:117], 2.0 op_sel_hi:[1,0] neg_lo:[1,0] neg_hi:[1,0]
	v_rcp_f32_e32 v114, v114
	v_rcp_f32_e32 v115, v115
	v_pk_add_f32 v[118:119], v[118:119], 2.0 op_sel_hi:[1,0] neg_lo:[1,0] neg_hi:[1,0]
	v_pk_mul_f32 v[112:113], v[112:113], v[116:117]
	v_pk_mul_f32 v[114:115], v[114:115], v[118:119]
	v_cvt_pk_fp8_f32 v124, v112, v113
	s_add_u32 s0, s8, s27
	s_addc_u32 s1, s9, 0
	s_ashr_i32 s35, s34, 31
	s_lshl_b64 s[34:35], s[34:35], 21
	v_ashrrev_i32_e32 v209, 31, v208
	s_add_u32 s36, s73, s34
	v_lshl_add_u64 v[122:123], s[0:1], 0, v[210:211]
	v_cvt_pk_fp8_f32 v124, v114, v115 op_sel:[0,0,1]
	v_lshlrev_b64 v[116:117], 10, v[208:209]
	s_addc_u32 s37, s74, s35
	v_lshl_add_u64 v[118:119], v[122:123], 0, v[116:117]
	global_store_dword v[118:119], v124, off
	s_cmp_eq_u32 s30, 7
	s_cselect_b64 s[34:35], -1, 0
	s_cmp_lg_u32 s30, 7
	v_lshl_add_u64 v[120:121], v[210:211], 1, s[36:37]
	v_exp_f32_e32 v104, v104
	v_exp_f32_e32 v105, v105
	v_exp_f32_e32 v106, v106
	v_pk_add_f32 v[104:105], v[104:105], 1.0 op_sel_hi:[1,0]
	v_exp_f32_e32 v107, v107
	v_exp_f32_e32 v108, v108
	v_pk_add_f32 v[106:107], v[106:107], 1.0 op_sel_hi:[1,0]
	v_exp_f32_e32 v109, v109
	v_exp_f32_e32 v110, v110
	v_pk_add_f32 v[108:109], v[108:109], 1.0 op_sel_hi:[1,0]
	v_exp_f32_e32 v111, v111
	v_exp_f32_e32 v100, v100
	v_pk_add_f32 v[110:111], v[110:111], 1.0 op_sel_hi:[1,0]
	v_exp_f32_e32 v101, v101
	v_pk_mul_f32 v[104:105], v[104:105], v[108:109]
	v_exp_f32_e32 v102, v102
	v_pk_mul_f32 v[106:107], v[106:107], v[110:111]
	v_exp_f32_e32 v103, v103
	v_pk_add_f32 v[100:101], v[100:101], 1.0 op_sel_hi:[1,0]
	v_rcp_f32_e32 v104, v104
	v_rcp_f32_e32 v105, v105
	v_pk_add_f32 v[102:103], v[102:103], 1.0 op_sel_hi:[1,0]
	v_rcp_f32_e32 v106, v106
	v_rcp_f32_e32 v107, v107
	v_pk_add_f32 v[108:109], v[108:109], 2.0 op_sel_hi:[1,0] neg_lo:[1,0] neg_hi:[1,0]
	v_rcp_f32_e32 v100, v100
	v_rcp_f32_e32 v101, v101
	v_pk_add_f32 v[110:111], v[110:111], 2.0 op_sel_hi:[1,0] neg_lo:[1,0] neg_hi:[1,0]
	v_rcp_f32_e32 v102, v102
	v_rcp_f32_e32 v103, v103
	v_pk_mul_f32 v[108:109], v[108:109], v[104:105]
	v_pk_mul_f32 v[110:111], v[110:111], v[106:107]
	s_waitcnt lgkmcnt(2)
	v_lshl_add_u64 v[104:105], v[176:177], 0, s[18:19]
	v_pk_fma_f32 v[100:101], v[168:169], v[100:101], v[108:109]
	v_pk_fma_f32 v[102:103], v[170:171], v[102:103], v[110:111]
	global_store_dwordx4 v[104:105], v[100:103], off sc1
	s_nop 1
	v_pk_mul_f32 v[100:101], v[100:101], s[96:97] op_sel_hi:[1,0]
	v_pk_mul_f32 v[102:103], v[102:103], s[96:97] op_sel_hi:[1,0]
	v_exp_f32_e32 v96, v96
	v_exp_f32_e32 v97, v97
	v_exp_f32_e32 v98, v98
	v_pk_fma_f32 v[96:97], v[96:97], s[98:99], s[98:99] op_sel_hi:[1,0,0]
	v_exp_f32_e32 v99, v99
	v_exp_f32_e32 v100, v100
	v_pk_fma_f32 v[98:99], v[98:99], s[98:99], s[98:99] op_sel_hi:[1,0,0]
	v_exp_f32_e32 v101, v101
	v_exp_f32_e32 v102, v102
	v_pk_add_f32 v[100:101], v[100:101], 1.0 op_sel_hi:[1,0]
	v_exp_f32_e32 v103, v103
	v_pk_mul_f32 v[96:97], v[96:97], v[100:101]
	v_rcp_f32_e32 v96, v96
	v_pk_add_f32 v[102:103], v[102:103], 1.0 op_sel_hi:[1,0]
	v_rcp_f32_e32 v97, v97
	v_pk_mul_f32 v[98:99], v[98:99], v[102:103]
	v_pk_add_f32 v[100:101], v[100:101], 2.0 op_sel_hi:[1,0] neg_lo:[1,0] neg_hi:[1,0]
	v_rcp_f32_e32 v98, v98
	v_rcp_f32_e32 v99, v99
	v_pk_add_f32 v[102:103], v[102:103], 2.0 op_sel_hi:[1,0] neg_lo:[1,0] neg_hi:[1,0]
	v_pk_mul_f32 v[96:97], v[96:97], v[100:101]
	v_pk_mul_f32 v[98:99], v[98:99], v[102:103]
	v_cvt_pk_fp8_f32 v104, v96, v97
	v_ashrrev_i32_e32 v207, 31, v206
	v_lshlrev_b64 v[100:101], 10, v[206:207]
	v_lshl_add_u64 v[102:103], v[122:123], 0, v[100:101]
	v_cvt_pk_fp8_f32 v104, v98, v99 op_sel:[0,0,1]
	v_cndmask_b32_e64 v105, 0, 1, s[34:35]
	global_store_dword v[102:103], v104, off
	v_cmp_ne_u32_e64 s[0:1], 1, v105
	v_exp_f32_e32 v88, v88
	v_exp_f32_e32 v89, v89
	v_exp_f32_e32 v90, v90
	v_pk_add_f32 v[88:89], v[88:89], 1.0 op_sel_hi:[1,0]
	v_exp_f32_e32 v91, v91
	v_exp_f32_e32 v92, v92
	v_pk_add_f32 v[90:91], v[90:91], 1.0 op_sel_hi:[1,0]
	v_exp_f32_e32 v93, v93
	v_exp_f32_e32 v94, v94
	v_pk_add_f32 v[92:93], v[92:93], 1.0 op_sel_hi:[1,0]
	v_exp_f32_e32 v95, v95
	v_exp_f32_e32 v84, v84
	v_pk_add_f32 v[94:95], v[94:95], 1.0 op_sel_hi:[1,0]
	v_exp_f32_e32 v85, v85
	v_pk_mul_f32 v[88:89], v[88:89], v[92:93]
	v_exp_f32_e32 v86, v86
	v_pk_mul_f32 v[90:91], v[90:91], v[94:95]
	v_exp_f32_e32 v87, v87
	v_pk_add_f32 v[84:85], v[84:85], 1.0 op_sel_hi:[1,0]
	v_rcp_f32_e32 v88, v88
	v_rcp_f32_e32 v89, v89
	v_pk_add_f32 v[86:87], v[86:87], 1.0 op_sel_hi:[1,0]
	v_rcp_f32_e32 v90, v90
	v_rcp_f32_e32 v91, v91
	v_pk_add_f32 v[92:93], v[92:93], 2.0 op_sel_hi:[1,0] neg_lo:[1,0] neg_hi:[1,0]
	v_rcp_f32_e32 v84, v84
	v_rcp_f32_e32 v85, v85
	v_pk_add_f32 v[94:95], v[94:95], 2.0 op_sel_hi:[1,0] neg_lo:[1,0] neg_hi:[1,0]
	v_rcp_f32_e32 v86, v86
	v_rcp_f32_e32 v87, v87
	v_pk_mul_f32 v[92:93], v[92:93], v[88:89]
	v_pk_mul_f32 v[94:95], v[94:95], v[90:91]
	s_waitcnt lgkmcnt(1)
	v_pk_fma_f32 v[84:85], v[164:165], v[84:85], v[92:93]
	v_pk_fma_f32 v[86:87], v[166:167], v[86:87], v[94:95]
	v_lshl_add_u64 v[88:89], v[176:177], 0, s[12:13]
	global_store_dwordx4 v[88:89], v[84:87], off sc1
	s_nop 1
	v_pk_mul_f32 v[84:85], v[84:85], s[96:97] op_sel_hi:[1,0]
	v_pk_mul_f32 v[86:87], v[86:87], s[96:97] op_sel_hi:[1,0]
	v_exp_f32_e32 v80, v80
	v_exp_f32_e32 v81, v81
	v_exp_f32_e32 v82, v82
	v_pk_fma_f32 v[80:81], v[80:81], s[98:99], s[98:99] op_sel_hi:[1,0,0]
	v_exp_f32_e32 v83, v83
	v_exp_f32_e32 v84, v84
	v_pk_fma_f32 v[82:83], v[82:83], s[98:99], s[98:99] op_sel_hi:[1,0,0]
	v_exp_f32_e32 v85, v85
	v_exp_f32_e32 v86, v86
	v_pk_add_f32 v[84:85], v[84:85], 1.0 op_sel_hi:[1,0]
	v_exp_f32_e32 v87, v87
	v_pk_mul_f32 v[80:81], v[80:81], v[84:85]
	v_rcp_f32_e32 v80, v80
	v_pk_add_f32 v[86:87], v[86:87], 1.0 op_sel_hi:[1,0]
	v_rcp_f32_e32 v81, v81
	v_pk_mul_f32 v[82:83], v[82:83], v[86:87]
	v_pk_add_f32 v[84:85], v[84:85], 2.0 op_sel_hi:[1,0] neg_lo:[1,0] neg_hi:[1,0]
	v_rcp_f32_e32 v82, v82
	v_rcp_f32_e32 v83, v83
	v_pk_add_f32 v[86:87], v[86:87], 2.0 op_sel_hi:[1,0] neg_lo:[1,0] neg_hi:[1,0]
	v_pk_mul_f32 v[80:81], v[80:81], v[84:85]
	v_pk_mul_f32 v[82:83], v[82:83], v[86:87]
	v_ashrrev_i32_e32 v205, 31, v204
	v_cvt_pk_fp8_f32 v88, v80, v81
	s_and_b64 vcc, exec, s[0:1]
	v_cvt_pk_fp8_f32 v88, v82, v83 op_sel:[0,0,1]
	v_lshlrev_b64 v[84:85], 10, v[204:205]
	v_lshl_add_u64 v[86:87], v[122:123], 0, v[84:85]
	global_store_dword v[86:87], v88, off
	v_exp_f32_e32 v72, v72
	v_exp_f32_e32 v73, v73
	v_exp_f32_e32 v74, v74
	v_pk_add_f32 v[72:73], v[72:73], 1.0 op_sel_hi:[1,0]
	v_exp_f32_e32 v75, v75
	v_exp_f32_e32 v76, v76
	v_pk_add_f32 v[74:75], v[74:75], 1.0 op_sel_hi:[1,0]
	v_exp_f32_e32 v77, v77
	v_exp_f32_e32 v78, v78
	v_pk_add_f32 v[76:77], v[76:77], 1.0 op_sel_hi:[1,0]
	v_exp_f32_e32 v79, v79
	v_exp_f32_e32 v68, v68
	v_pk_add_f32 v[78:79], v[78:79], 1.0 op_sel_hi:[1,0]
	v_exp_f32_e32 v69, v69
	v_pk_mul_f32 v[72:73], v[72:73], v[76:77]
	v_exp_f32_e32 v70, v70
	v_pk_mul_f32 v[74:75], v[74:75], v[78:79]
	v_exp_f32_e32 v71, v71
	v_pk_add_f32 v[68:69], v[68:69], 1.0 op_sel_hi:[1,0]
	v_rcp_f32_e32 v72, v72
	v_rcp_f32_e32 v73, v73
	v_pk_add_f32 v[70:71], v[70:71], 1.0 op_sel_hi:[1,0]
	v_rcp_f32_e32 v74, v74
	v_rcp_f32_e32 v75, v75
	v_pk_add_f32 v[76:77], v[76:77], 2.0 op_sel_hi:[1,0] neg_lo:[1,0] neg_hi:[1,0]
	v_rcp_f32_e32 v68, v68
	v_rcp_f32_e32 v69, v69
	v_pk_add_f32 v[78:79], v[78:79], 2.0 op_sel_hi:[1,0] neg_lo:[1,0] neg_hi:[1,0]
	v_rcp_f32_e32 v70, v70
	v_rcp_f32_e32 v71, v71
	v_pk_mul_f32 v[76:77], v[76:77], v[72:73]
	v_pk_mul_f32 v[78:79], v[78:79], v[74:75]
	s_waitcnt lgkmcnt(0)
	v_lshl_add_u64 v[72:73], v[176:177], 0, s[20:21]
	v_pk_fma_f32 v[68:69], v[160:161], v[68:69], v[76:77]
	v_pk_fma_f32 v[70:71], v[162:163], v[70:71], v[78:79]
	global_store_dwordx4 v[72:73], v[68:71], off sc1
	s_nop 1
	v_pk_mul_f32 v[68:69], v[68:69], s[96:97] op_sel_hi:[1,0]
	v_pk_mul_f32 v[70:71], v[70:71], s[96:97] op_sel_hi:[1,0]
	v_exp_f32_e32 v64, v64
	v_exp_f32_e32 v65, v65
	v_exp_f32_e32 v66, v66
	v_pk_fma_f32 v[64:65], v[64:65], s[98:99], s[98:99] op_sel_hi:[1,0,0]
	v_exp_f32_e32 v67, v67
	v_exp_f32_e32 v68, v68
	v_pk_fma_f32 v[66:67], v[66:67], s[98:99], s[98:99] op_sel_hi:[1,0,0]
	v_exp_f32_e32 v69, v69
	v_exp_f32_e32 v70, v70
	v_pk_add_f32 v[68:69], v[68:69], 1.0 op_sel_hi:[1,0]
	v_exp_f32_e32 v71, v71
	v_pk_mul_f32 v[64:65], v[64:65], v[68:69]
	v_rcp_f32_e32 v64, v64
	v_pk_add_f32 v[70:71], v[70:71], 1.0 op_sel_hi:[1,0]
	v_rcp_f32_e32 v65, v65
	v_pk_mul_f32 v[66:67], v[66:67], v[70:71]
	v_pk_add_f32 v[68:69], v[68:69], 2.0 op_sel_hi:[1,0] neg_lo:[1,0] neg_hi:[1,0]
	v_rcp_f32_e32 v66, v66
	v_rcp_f32_e32 v67, v67
	v_pk_add_f32 v[70:71], v[70:71], 2.0 op_sel_hi:[1,0] neg_lo:[1,0] neg_hi:[1,0]
	v_pk_mul_f32 v[64:65], v[64:65], v[68:69]
	v_pk_mul_f32 v[66:67], v[66:67], v[70:71]
	v_ashrrev_i32_e32 v203, 31, v202
	v_cvt_pk_fp8_f32 v72, v64, v65
	s_and_b64 vcc, exec, s[0:1]
	v_cvt_pk_fp8_f32 v72, v66, v67 op_sel:[0,0,1]
	v_lshlrev_b64 v[68:69], 10, v[202:203]
	v_lshl_add_u64 v[70:71], v[122:123], 0, v[68:69]
	global_store_dword v[70:71], v72, off
	v_exp_f32_e32 v56, v56
	v_exp_f32_e32 v57, v57
	v_exp_f32_e32 v58, v58
	v_pk_add_f32 v[56:57], v[56:57], 1.0 op_sel_hi:[1,0]
	v_exp_f32_e32 v59, v59
	v_exp_f32_e32 v60, v60
	v_pk_add_f32 v[58:59], v[58:59], 1.0 op_sel_hi:[1,0]
	v_exp_f32_e32 v61, v61
	v_exp_f32_e32 v62, v62
	v_pk_add_f32 v[60:61], v[60:61], 1.0 op_sel_hi:[1,0]
	v_exp_f32_e32 v63, v63
	v_exp_f32_e32 v52, v52
	v_pk_add_f32 v[62:63], v[62:63], 1.0 op_sel_hi:[1,0]
	v_exp_f32_e32 v53, v53
	v_pk_mul_f32 v[56:57], v[56:57], v[60:61]
	v_exp_f32_e32 v54, v54
	v_pk_mul_f32 v[58:59], v[58:59], v[62:63]
	v_exp_f32_e32 v55, v55
	v_pk_add_f32 v[52:53], v[52:53], 1.0 op_sel_hi:[1,0]
	v_rcp_f32_e32 v56, v56
	v_rcp_f32_e32 v57, v57
	v_pk_add_f32 v[54:55], v[54:55], 1.0 op_sel_hi:[1,0]
	v_rcp_f32_e32 v58, v58
	v_rcp_f32_e32 v59, v59
	v_pk_add_f32 v[60:61], v[60:61], 2.0 op_sel_hi:[1,0] neg_lo:[1,0] neg_hi:[1,0]
	v_rcp_f32_e32 v52, v52
	v_rcp_f32_e32 v53, v53
	v_pk_add_f32 v[62:63], v[62:63], 2.0 op_sel_hi:[1,0] neg_lo:[1,0] neg_hi:[1,0]
	v_rcp_f32_e32 v54, v54
	v_rcp_f32_e32 v55, v55
	v_pk_mul_f32 v[60:61], v[60:61], v[56:57]
	v_pk_mul_f32 v[62:63], v[62:63], v[58:59]
	s_waitcnt vmcnt(8)
	v_pk_fma_f32 v[52:53], v[156:157], v[52:53], v[60:61]
	v_pk_fma_f32 v[54:55], v[158:159], v[54:55], v[62:63]
	v_lshl_add_u64 v[56:57], v[176:177], 0, s[14:15]
	global_store_dwordx4 v[56:57], v[52:55], off sc1
	s_nop 1
	v_pk_mul_f32 v[52:53], v[52:53], s[96:97] op_sel_hi:[1,0]
	v_pk_mul_f32 v[54:55], v[54:55], s[96:97] op_sel_hi:[1,0]
	v_exp_f32_e32 v48, v48
	v_exp_f32_e32 v49, v49
	v_exp_f32_e32 v50, v50
	v_pk_fma_f32 v[48:49], v[48:49], s[98:99], s[98:99] op_sel_hi:[1,0,0]
	v_exp_f32_e32 v51, v51
	v_exp_f32_e32 v52, v52
	v_pk_fma_f32 v[50:51], v[50:51], s[98:99], s[98:99] op_sel_hi:[1,0,0]
	v_exp_f32_e32 v53, v53
	v_exp_f32_e32 v54, v54
	v_pk_add_f32 v[52:53], v[52:53], 1.0 op_sel_hi:[1,0]
	v_exp_f32_e32 v55, v55
	v_pk_mul_f32 v[48:49], v[48:49], v[52:53]
	v_rcp_f32_e32 v48, v48
	v_pk_add_f32 v[54:55], v[54:55], 1.0 op_sel_hi:[1,0]
	v_rcp_f32_e32 v49, v49
	v_pk_mul_f32 v[50:51], v[50:51], v[54:55]
	v_pk_add_f32 v[52:53], v[52:53], 2.0 op_sel_hi:[1,0] neg_lo:[1,0] neg_hi:[1,0]
	v_rcp_f32_e32 v50, v50
	v_rcp_f32_e32 v51, v51
	v_pk_add_f32 v[54:55], v[54:55], 2.0 op_sel_hi:[1,0] neg_lo:[1,0] neg_hi:[1,0]
	v_pk_mul_f32 v[48:49], v[48:49], v[52:53]
	v_pk_mul_f32 v[50:51], v[50:51], v[54:55]
	v_ashrrev_i32_e32 v201, 31, v200
	v_cvt_pk_fp8_f32 v56, v48, v49
	s_and_b64 vcc, exec, s[0:1]
	v_cvt_pk_fp8_f32 v56, v50, v51 op_sel:[0,0,1]
	v_lshlrev_b64 v[52:53], 10, v[200:201]
	v_lshl_add_u64 v[54:55], v[122:123], 0, v[52:53]
	global_store_dword v[54:55], v56, off
	v_exp_f32_e32 v40, v40
	v_exp_f32_e32 v41, v41
	v_exp_f32_e32 v42, v42
	v_pk_add_f32 v[40:41], v[40:41], 1.0 op_sel_hi:[1,0]
	v_exp_f32_e32 v43, v43
	v_exp_f32_e32 v44, v44
	v_pk_add_f32 v[42:43], v[42:43], 1.0 op_sel_hi:[1,0]
	v_exp_f32_e32 v45, v45
	v_exp_f32_e32 v46, v46
	v_pk_add_f32 v[44:45], v[44:45], 1.0 op_sel_hi:[1,0]
	v_exp_f32_e32 v47, v47
	v_exp_f32_e32 v36, v36
	v_pk_add_f32 v[46:47], v[46:47], 1.0 op_sel_hi:[1,0]
	v_exp_f32_e32 v37, v37
	v_pk_mul_f32 v[40:41], v[40:41], v[44:45]
	v_exp_f32_e32 v38, v38
	v_pk_mul_f32 v[42:43], v[42:43], v[46:47]
	v_exp_f32_e32 v39, v39
	v_pk_add_f32 v[36:37], v[36:37], 1.0 op_sel_hi:[1,0]
	v_rcp_f32_e32 v40, v40
	v_rcp_f32_e32 v41, v41
	v_pk_add_f32 v[38:39], v[38:39], 1.0 op_sel_hi:[1,0]
	v_rcp_f32_e32 v42, v42
	v_rcp_f32_e32 v43, v43
	v_pk_add_f32 v[44:45], v[44:45], 2.0 op_sel_hi:[1,0] neg_lo:[1,0] neg_hi:[1,0]
	v_rcp_f32_e32 v36, v36
	v_rcp_f32_e32 v37, v37
	v_pk_add_f32 v[46:47], v[46:47], 2.0 op_sel_hi:[1,0] neg_lo:[1,0] neg_hi:[1,0]
	v_rcp_f32_e32 v38, v38
	v_rcp_f32_e32 v39, v39
	v_pk_mul_f32 v[44:45], v[44:45], v[40:41]
	v_pk_mul_f32 v[46:47], v[46:47], v[42:43]
	v_lshl_add_u64 v[40:41], v[176:177], 0, s[22:23]
	v_pk_fma_f32 v[36:37], v[152:153], v[36:37], v[44:45]
	v_pk_fma_f32 v[38:39], v[154:155], v[38:39], v[46:47]
	global_store_dwordx4 v[40:41], v[36:39], off sc1
	s_nop 1
	v_pk_mul_f32 v[36:37], v[36:37], s[96:97] op_sel_hi:[1,0]
	v_pk_mul_f32 v[38:39], v[38:39], s[96:97] op_sel_hi:[1,0]
	v_exp_f32_e32 v32, v32
	v_exp_f32_e32 v33, v33
	v_exp_f32_e32 v34, v34
	v_pk_fma_f32 v[32:33], v[32:33], s[98:99], s[98:99] op_sel_hi:[1,0,0]
	v_exp_f32_e32 v35, v35
	v_exp_f32_e32 v36, v36
	v_pk_fma_f32 v[34:35], v[34:35], s[98:99], s[98:99] op_sel_hi:[1,0,0]
	v_exp_f32_e32 v37, v37
	v_exp_f32_e32 v38, v38
	v_pk_add_f32 v[36:37], v[36:37], 1.0 op_sel_hi:[1,0]
	v_exp_f32_e32 v39, v39
	v_pk_mul_f32 v[32:33], v[32:33], v[36:37]
	v_rcp_f32_e32 v32, v32
	v_pk_add_f32 v[38:39], v[38:39], 1.0 op_sel_hi:[1,0]
	v_rcp_f32_e32 v33, v33
	v_pk_mul_f32 v[34:35], v[34:35], v[38:39]
	v_pk_add_f32 v[36:37], v[36:37], 2.0 op_sel_hi:[1,0] neg_lo:[1,0] neg_hi:[1,0]
	v_rcp_f32_e32 v34, v34
	v_rcp_f32_e32 v35, v35
	v_pk_add_f32 v[38:39], v[38:39], 2.0 op_sel_hi:[1,0] neg_lo:[1,0] neg_hi:[1,0]
	v_pk_mul_f32 v[32:33], v[32:33], v[36:37]
	v_pk_mul_f32 v[34:35], v[34:35], v[38:39]
	v_cvt_pk_fp8_f32 v40, v32, v33
	v_or_b32_e32 v36, 16, v200
	v_ashrrev_i32_e32 v37, 31, v36
	v_lshlrev_b64 v[36:37], 10, v[36:37]
	v_cvt_pk_fp8_f32 v40, v34, v35 op_sel:[0,0,1]
	v_lshl_add_u64 v[38:39], v[122:123], 0, v[36:37]
	global_store_dword v[38:39], v40, off
	v_exp_f32_e32 v24, v24
	v_exp_f32_e32 v25, v25
	v_exp_f32_e32 v26, v26
	v_pk_add_f32 v[24:25], v[24:25], 1.0 op_sel_hi:[1,0]
	v_exp_f32_e32 v27, v27
	v_exp_f32_e32 v28, v28
	v_pk_add_f32 v[26:27], v[26:27], 1.0 op_sel_hi:[1,0]
	v_exp_f32_e32 v29, v29
	v_exp_f32_e32 v30, v30
	v_pk_add_f32 v[28:29], v[28:29], 1.0 op_sel_hi:[1,0]
	v_exp_f32_e32 v31, v31
	v_exp_f32_e32 v20, v20
	v_pk_add_f32 v[30:31], v[30:31], 1.0 op_sel_hi:[1,0]
	v_exp_f32_e32 v21, v21
	v_pk_mul_f32 v[24:25], v[24:25], v[28:29]
	v_exp_f32_e32 v22, v22
	v_pk_mul_f32 v[26:27], v[26:27], v[30:31]
	v_exp_f32_e32 v23, v23
	v_pk_add_f32 v[20:21], v[20:21], 1.0 op_sel_hi:[1,0]
	v_rcp_f32_e32 v24, v24
	v_rcp_f32_e32 v25, v25
	v_pk_add_f32 v[22:23], v[22:23], 1.0 op_sel_hi:[1,0]
	v_rcp_f32_e32 v26, v26
	v_rcp_f32_e32 v27, v27
	v_pk_add_f32 v[28:29], v[28:29], 2.0 op_sel_hi:[1,0] neg_lo:[1,0] neg_hi:[1,0]
	v_rcp_f32_e32 v20, v20
	v_rcp_f32_e32 v21, v21
	v_pk_add_f32 v[30:31], v[30:31], 2.0 op_sel_hi:[1,0] neg_lo:[1,0] neg_hi:[1,0]
	v_rcp_f32_e32 v22, v22
	v_rcp_f32_e32 v23, v23
	v_pk_mul_f32 v[28:29], v[28:29], v[24:25]
	v_pk_mul_f32 v[30:31], v[30:31], v[26:27]
	v_pk_fma_f32 v[20:21], v[148:149], v[20:21], v[28:29]
	v_pk_fma_f32 v[22:23], v[150:151], v[22:23], v[30:31]
	v_lshl_add_u64 v[24:25], v[176:177], 0, s[16:17]
	global_store_dwordx4 v[24:25], v[20:23], off sc1
	s_nop 1
	v_pk_mul_f32 v[20:21], v[20:21], s[96:97] op_sel_hi:[1,0]
	v_pk_mul_f32 v[22:23], v[22:23], s[96:97] op_sel_hi:[1,0]
	v_exp_f32_e32 v16, v16
	v_exp_f32_e32 v17, v17
	v_exp_f32_e32 v18, v18
	v_pk_fma_f32 v[16:17], v[16:17], s[98:99], s[98:99] op_sel_hi:[1,0,0]
	v_exp_f32_e32 v19, v19
	v_exp_f32_e32 v20, v20
	v_pk_fma_f32 v[18:19], v[18:19], s[98:99], s[98:99] op_sel_hi:[1,0,0]
	v_exp_f32_e32 v21, v21
	v_exp_f32_e32 v22, v22
	v_pk_add_f32 v[20:21], v[20:21], 1.0 op_sel_hi:[1,0]
	v_exp_f32_e32 v23, v23
	v_pk_mul_f32 v[16:17], v[16:17], v[20:21]
	v_rcp_f32_e32 v16, v16
	v_pk_add_f32 v[22:23], v[22:23], 1.0 op_sel_hi:[1,0]
	v_rcp_f32_e32 v17, v17
	v_pk_mul_f32 v[18:19], v[18:19], v[22:23]
	v_pk_add_f32 v[20:21], v[20:21], 2.0 op_sel_hi:[1,0] neg_lo:[1,0] neg_hi:[1,0]
	v_rcp_f32_e32 v18, v18
	v_rcp_f32_e32 v19, v19
	v_pk_add_f32 v[22:23], v[22:23], 2.0 op_sel_hi:[1,0] neg_lo:[1,0] neg_hi:[1,0]
	v_pk_mul_f32 v[16:17], v[16:17], v[20:21]
	v_pk_mul_f32 v[18:19], v[18:19], v[22:23]
	v_cvt_pk_fp8_f32 v24, v16, v17
	v_or_b32_e32 v20, 32, v200
	v_ashrrev_i32_e32 v21, 31, v20
	v_lshlrev_b64 v[20:21], 10, v[20:21]
	v_cvt_pk_fp8_f32 v24, v18, v19 op_sel:[0,0,1]
	v_lshl_add_u64 v[22:23], v[122:123], 0, v[20:21]
	global_store_dword v[22:23], v24, off
	v_exp_f32_e32 v8, v8
	v_exp_f32_e32 v9, v9
	v_exp_f32_e32 v10, v10
	v_pk_add_f32 v[8:9], v[8:9], 1.0 op_sel_hi:[1,0]
	v_exp_f32_e32 v11, v11
	v_exp_f32_e32 v12, v12
	v_pk_add_f32 v[10:11], v[10:11], 1.0 op_sel_hi:[1,0]
	v_exp_f32_e32 v13, v13
	v_exp_f32_e32 v14, v14
	v_pk_add_f32 v[12:13], v[12:13], 1.0 op_sel_hi:[1,0]
	v_exp_f32_e32 v15, v15
	v_exp_f32_e32 v4, v4
	v_pk_add_f32 v[14:15], v[14:15], 1.0 op_sel_hi:[1,0]
	v_exp_f32_e32 v5, v5
	v_pk_mul_f32 v[8:9], v[8:9], v[12:13]
	v_exp_f32_e32 v6, v6
	v_pk_mul_f32 v[10:11], v[10:11], v[14:15]
	v_exp_f32_e32 v7, v7
	v_pk_add_f32 v[4:5], v[4:5], 1.0 op_sel_hi:[1,0]
	v_rcp_f32_e32 v8, v8
	v_rcp_f32_e32 v9, v9
	v_pk_add_f32 v[6:7], v[6:7], 1.0 op_sel_hi:[1,0]
	v_rcp_f32_e32 v10, v10
	v_rcp_f32_e32 v11, v11
	v_pk_add_f32 v[12:13], v[12:13], 2.0 op_sel_hi:[1,0] neg_lo:[1,0] neg_hi:[1,0]
	v_rcp_f32_e32 v4, v4
	v_rcp_f32_e32 v5, v5
	v_pk_add_f32 v[14:15], v[14:15], 2.0 op_sel_hi:[1,0] neg_lo:[1,0] neg_hi:[1,0]
	v_rcp_f32_e32 v6, v6
	v_rcp_f32_e32 v7, v7
	v_pk_mul_f32 v[12:13], v[12:13], v[8:9]
	v_pk_mul_f32 v[14:15], v[14:15], v[10:11]
	v_lshl_add_u64 v[8:9], v[176:177], 0, s[24:25]
	v_pk_fma_f32 v[4:5], v[144:145], v[4:5], v[12:13]
	v_pk_fma_f32 v[6:7], v[146:147], v[6:7], v[14:15]
	global_store_dwordx4 v[8:9], v[4:7], off sc1
	s_nop 1
	v_pk_mul_f32 v[4:5], v[4:5], s[96:97] op_sel_hi:[1,0]
	v_pk_mul_f32 v[6:7], v[6:7], s[96:97] op_sel_hi:[1,0]
	v_exp_f32_e32 v0, v0
	v_exp_f32_e32 v1, v1
	v_exp_f32_e32 v2, v2
	v_pk_fma_f32 v[0:1], v[0:1], s[98:99], s[98:99] op_sel_hi:[1,0,0]
	v_exp_f32_e32 v3, v3
	v_exp_f32_e32 v4, v4
	v_pk_fma_f32 v[2:3], v[2:3], s[98:99], s[98:99] op_sel_hi:[1,0,0]
	v_exp_f32_e32 v5, v5
	v_exp_f32_e32 v6, v6
	v_pk_add_f32 v[4:5], v[4:5], 1.0 op_sel_hi:[1,0]
	v_exp_f32_e32 v7, v7
	v_pk_mul_f32 v[0:1], v[0:1], v[4:5]
	v_rcp_f32_e32 v0, v0
	v_pk_add_f32 v[6:7], v[6:7], 1.0 op_sel_hi:[1,0]
	v_rcp_f32_e32 v1, v1
	v_pk_mul_f32 v[2:3], v[2:3], v[6:7]
	v_pk_add_f32 v[4:5], v[4:5], 2.0 op_sel_hi:[1,0] neg_lo:[1,0] neg_hi:[1,0]
	v_rcp_f32_e32 v2, v2
	v_rcp_f32_e32 v3, v3
	v_pk_add_f32 v[6:7], v[6:7], 2.0 op_sel_hi:[1,0] neg_lo:[1,0] neg_hi:[1,0]
	v_pk_mul_f32 v[0:1], v[0:1], v[4:5]
	v_pk_mul_f32 v[2:3], v[2:3], v[6:7]
	v_cvt_pk_fp8_f32 v8, v0, v1
	v_or_b32_e32 v4, 48, v200
	v_ashrrev_i32_e32 v5, 31, v4
	v_lshlrev_b64 v[4:5], 10, v[4:5]
	v_cvt_pk_fp8_f32 v8, v2, v3 op_sel:[0,0,1]
	v_lshl_add_u64 v[6:7], v[122:123], 0, v[4:5]
	global_store_dword v[6:7], v8, off
	s_branch .LBB2_24
.Lmy_epi_l7:
	v_exp_f32_e32 v120, v120
	v_exp_f32_e32 v121, v121
	v_exp_f32_e32 v122, v122
	v_pk_add_f32 v[120:121], v[120:121], 1.0 op_sel_hi:[1,0]
	v_exp_f32_e32 v123, v123
	v_exp_f32_e32 v124, v124
	v_pk_add_f32 v[122:123], v[122:123], 1.0 op_sel_hi:[1,0]
	v_exp_f32_e32 v125, v125
	v_exp_f32_e32 v126, v126
	v_pk_add_f32 v[124:125], v[124:125], 1.0 op_sel_hi:[1,0]
	v_exp_f32_e32 v127, v127
	v_exp_f32_e32 v116, v116
	v_pk_add_f32 v[126:127], v[126:127], 1.0 op_sel_hi:[1,0]
	v_exp_f32_e32 v117, v117
	v_pk_mul_f32 v[120:121], v[120:121], v[124:125]
	v_exp_f32_e32 v118, v118
	v_pk_mul_f32 v[122:123], v[122:123], v[126:127]
	v_exp_f32_e32 v119, v119
	v_pk_add_f32 v[116:117], v[116:117], 1.0 op_sel_hi:[1,0]
	v_rcp_f32_e32 v120, v120
	v_rcp_f32_e32 v121, v121
	v_pk_add_f32 v[118:119], v[118:119], 1.0 op_sel_hi:[1,0]
	v_rcp_f32_e32 v122, v122
	v_rcp_f32_e32 v123, v123
	v_pk_add_f32 v[124:125], v[124:125], 2.0 op_sel_hi:[1,0] neg_lo:[1,0] neg_hi:[1,0]
	v_rcp_f32_e32 v116, v116
	v_rcp_f32_e32 v117, v117
	v_pk_add_f32 v[126:127], v[126:127], 2.0 op_sel_hi:[1,0] neg_lo:[1,0] neg_hi:[1,0]
	v_rcp_f32_e32 v118, v118
	v_rcp_f32_e32 v119, v119
	v_pk_mul_f32 v[124:125], v[124:125], v[120:121]
	v_pk_mul_f32 v[126:127], v[126:127], v[122:123]
	s_waitcnt lgkmcnt(3)
	v_pk_fma_f32 v[116:117], v[172:173], v[116:117], v[124:125]
	v_pk_fma_f32 v[118:119], v[174:175], v[118:119], v[126:127]
	global_store_dwordx4 v[176:177], v[116:119], off sc1
	s_nop 1
	v_pk_mul_f32 v[116:117], v[116:117], s[96:97] op_sel_hi:[1,0]
	v_pk_mul_f32 v[118:119], v[118:119], s[96:97] op_sel_hi:[1,0]
	v_exp_f32_e32 v112, v112
	v_exp_f32_e32 v113, v113
	v_exp_f32_e32 v114, v114
	v_pk_fma_f32 v[112:113], v[112:113], s[98:99], s[98:99] op_sel_hi:[1,0,0]
	v_exp_f32_e32 v115, v115
	v_exp_f32_e32 v116, v116
	v_pk_fma_f32 v[114:115], v[114:115], s[98:99], s[98:99] op_sel_hi:[1,0,0]
	v_exp_f32_e32 v117, v117
	v_exp_f32_e32 v118, v118
	v_pk_add_f32 v[116:117], v[116:117], 1.0 op_sel_hi:[1,0]
	v_exp_f32_e32 v119, v119
	v_pk_mul_f32 v[112:113], v[112:113], v[116:117]
	v_rcp_f32_e32 v112, v112
	v_pk_add_f32 v[118:119], v[118:119], 1.0 op_sel_hi:[1,0]
	v_rcp_f32_e32 v113, v113
	v_pk_mul_f32 v[114:115], v[114:115], v[118:119]
	v_pk_add_f32 v[116:117], v[116:117], 2.0 op_sel_hi:[1,0] neg_lo:[1,0] neg_hi:[1,0]
	v_rcp_f32_e32 v114, v114
	v_rcp_f32_e32 v115, v115
	v_pk_add_f32 v[118:119], v[118:119], 2.0 op_sel_hi:[1,0] neg_lo:[1,0] neg_hi:[1,0]
	v_pk_mul_f32 v[112:113], v[112:113], v[116:117]
	v_pk_mul_f32 v[114:115], v[114:115], v[118:119]
	v_cvt_pk_fp8_f32 v124, v112, v113
	s_add_u32 s0, s8, s27
	s_addc_u32 s1, s9, 0
	s_ashr_i32 s35, s34, 31
	s_lshl_b64 s[34:35], s[34:35], 21
	v_ashrrev_i32_e32 v209, 31, v208
	s_add_u32 s36, s73, s34
	v_lshl_add_u64 v[122:123], s[0:1], 0, v[210:211]
	v_cvt_pk_fp8_f32 v124, v114, v115 op_sel:[0,0,1]
	v_lshlrev_b64 v[116:117], 10, v[208:209]
	s_addc_u32 s37, s74, s35
	v_lshl_add_u64 v[118:119], v[122:123], 0, v[116:117]
	global_store_dword v[118:119], v124, off
	s_cmp_eq_u32 s30, 7
	s_cselect_b64 s[34:35], -1, 0
	s_cmp_lg_u32 s30, 7
	v_lshl_add_u64 v[120:121], v[210:211], 1, s[36:37]
	v_pk_mul_f32 v[112:113], v[112:113], s[98:99] op_sel_hi:[1,0]
	v_pk_mul_f32 v[114:115], v[114:115], s[98:99] op_sel_hi:[1,0]
	v_cvt_pk_f16_f32 v112, v112, v113
	v_cvt_pk_f16_f32 v113, v114, v115
	v_lshl_add_u64 v[114:115], v[116:117], 1, v[120:121]
	global_store_dwordx2 v[114:115], v[112:113], off
	v_exp_f32_e32 v104, v104
	v_exp_f32_e32 v105, v105
	v_exp_f32_e32 v106, v106
	v_pk_add_f32 v[104:105], v[104:105], 1.0 op_sel_hi:[1,0]
	v_exp_f32_e32 v107, v107
	v_exp_f32_e32 v108, v108
	v_pk_add_f32 v[106:107], v[106:107], 1.0 op_sel_hi:[1,0]
	v_exp_f32_e32 v109, v109
	v_exp_f32_e32 v110, v110
	v_pk_add_f32 v[108:109], v[108:109], 1.0 op_sel_hi:[1,0]
	v_exp_f32_e32 v111, v111
	v_exp_f32_e32 v100, v100
	v_pk_add_f32 v[110:111], v[110:111], 1.0 op_sel_hi:[1,0]
	v_exp_f32_e32 v101, v101
	v_pk_mul_f32 v[104:105], v[104:105], v[108:109]
	v_exp_f32_e32 v102, v102
	v_pk_mul_f32 v[106:107], v[106:107], v[110:111]
	v_exp_f32_e32 v103, v103
	v_pk_add_f32 v[100:101], v[100:101], 1.0 op_sel_hi:[1,0]
	v_rcp_f32_e32 v104, v104
	v_rcp_f32_e32 v105, v105
	v_pk_add_f32 v[102:103], v[102:103], 1.0 op_sel_hi:[1,0]
	v_rcp_f32_e32 v106, v106
	v_rcp_f32_e32 v107, v107
	v_pk_add_f32 v[108:109], v[108:109], 2.0 op_sel_hi:[1,0] neg_lo:[1,0] neg_hi:[1,0]
	v_rcp_f32_e32 v100, v100
	v_rcp_f32_e32 v101, v101
	v_pk_add_f32 v[110:111], v[110:111], 2.0 op_sel_hi:[1,0] neg_lo:[1,0] neg_hi:[1,0]
	v_rcp_f32_e32 v102, v102
	v_rcp_f32_e32 v103, v103
	v_pk_mul_f32 v[108:109], v[108:109], v[104:105]
	v_pk_mul_f32 v[110:111], v[110:111], v[106:107]
	s_waitcnt lgkmcnt(2)
	v_lshl_add_u64 v[104:105], v[176:177], 0, s[18:19]
	v_pk_fma_f32 v[100:101], v[168:169], v[100:101], v[108:109]
	v_pk_fma_f32 v[102:103], v[170:171], v[102:103], v[110:111]
	global_store_dwordx4 v[104:105], v[100:103], off sc1
	s_nop 1
	v_pk_mul_f32 v[100:101], v[100:101], s[96:97] op_sel_hi:[1,0]
	v_pk_mul_f32 v[102:103], v[102:103], s[96:97] op_sel_hi:[1,0]
	v_exp_f32_e32 v96, v96
	v_exp_f32_e32 v97, v97
	v_exp_f32_e32 v98, v98
	v_pk_fma_f32 v[96:97], v[96:97], s[98:99], s[98:99] op_sel_hi:[1,0,0]
	v_exp_f32_e32 v99, v99
	v_exp_f32_e32 v100, v100
	v_pk_fma_f32 v[98:99], v[98:99], s[98:99], s[98:99] op_sel_hi:[1,0,0]
	v_exp_f32_e32 v101, v101
	v_exp_f32_e32 v102, v102
	v_pk_add_f32 v[100:101], v[100:101], 1.0 op_sel_hi:[1,0]
	v_exp_f32_e32 v103, v103
	v_pk_mul_f32 v[96:97], v[96:97], v[100:101]
	v_rcp_f32_e32 v96, v96
	v_pk_add_f32 v[102:103], v[102:103], 1.0 op_sel_hi:[1,0]
	v_rcp_f32_e32 v97, v97
	v_pk_mul_f32 v[98:99], v[98:99], v[102:103]
	v_pk_add_f32 v[100:101], v[100:101], 2.0 op_sel_hi:[1,0] neg_lo:[1,0] neg_hi:[1,0]
	v_rcp_f32_e32 v98, v98
	v_rcp_f32_e32 v99, v99
	v_pk_add_f32 v[102:103], v[102:103], 2.0 op_sel_hi:[1,0] neg_lo:[1,0] neg_hi:[1,0]
	v_pk_mul_f32 v[96:97], v[96:97], v[100:101]
	v_pk_mul_f32 v[98:99], v[98:99], v[102:103]
	v_cvt_pk_fp8_f32 v104, v96, v97
	v_ashrrev_i32_e32 v207, 31, v206
	v_lshlrev_b64 v[100:101], 10, v[206:207]
	v_lshl_add_u64 v[102:103], v[122:123], 0, v[100:101]
	v_cvt_pk_fp8_f32 v104, v98, v99 op_sel:[0,0,1]
	v_cndmask_b32_e64 v105, 0, 1, s[34:35]
	global_store_dword v[102:103], v104, off
	v_cmp_ne_u32_e64 s[0:1], 1, v105
	v_pk_mul_f32 v[96:97], v[96:97], s[98:99] op_sel_hi:[1,0]
	v_pk_mul_f32 v[98:99], v[98:99], s[98:99] op_sel_hi:[1,0]
	v_cvt_pk_f16_f32 v96, v96, v97
	v_cvt_pk_f16_f32 v97, v98, v99
	v_lshl_add_u64 v[98:99], v[100:101], 1, v[120:121]
	global_store_dwordx2 v[98:99], v[96:97], off
	v_exp_f32_e32 v88, v88
	v_exp_f32_e32 v89, v89
	v_exp_f32_e32 v90, v90
	v_pk_add_f32 v[88:89], v[88:89], 1.0 op_sel_hi:[1,0]
	v_exp_f32_e32 v91, v91
	v_exp_f32_e32 v92, v92
	v_pk_add_f32 v[90:91], v[90:91], 1.0 op_sel_hi:[1,0]
	v_exp_f32_e32 v93, v93
	v_exp_f32_e32 v94, v94
	v_pk_add_f32 v[92:93], v[92:93], 1.0 op_sel_hi:[1,0]
	v_exp_f32_e32 v95, v95
	v_exp_f32_e32 v84, v84
	v_pk_add_f32 v[94:95], v[94:95], 1.0 op_sel_hi:[1,0]
	v_exp_f32_e32 v85, v85
	v_pk_mul_f32 v[88:89], v[88:89], v[92:93]
	v_exp_f32_e32 v86, v86
	v_pk_mul_f32 v[90:91], v[90:91], v[94:95]
	v_exp_f32_e32 v87, v87
	v_pk_add_f32 v[84:85], v[84:85], 1.0 op_sel_hi:[1,0]
	v_rcp_f32_e32 v88, v88
	v_rcp_f32_e32 v89, v89
	v_pk_add_f32 v[86:87], v[86:87], 1.0 op_sel_hi:[1,0]
	v_rcp_f32_e32 v90, v90
	v_rcp_f32_e32 v91, v91
	v_pk_add_f32 v[92:93], v[92:93], 2.0 op_sel_hi:[1,0] neg_lo:[1,0] neg_hi:[1,0]
	v_rcp_f32_e32 v84, v84
	v_rcp_f32_e32 v85, v85
	v_pk_add_f32 v[94:95], v[94:95], 2.0 op_sel_hi:[1,0] neg_lo:[1,0] neg_hi:[1,0]
	v_rcp_f32_e32 v86, v86
	v_rcp_f32_e32 v87, v87
	v_pk_mul_f32 v[92:93], v[92:93], v[88:89]
	v_pk_mul_f32 v[94:95], v[94:95], v[90:91]
	s_waitcnt lgkmcnt(1)
	v_pk_fma_f32 v[84:85], v[164:165], v[84:85], v[92:93]
	v_pk_fma_f32 v[86:87], v[166:167], v[86:87], v[94:95]
	v_lshl_add_u64 v[88:89], v[176:177], 0, s[12:13]
	global_store_dwordx4 v[88:89], v[84:87], off sc1
	s_nop 1
	v_pk_mul_f32 v[84:85], v[84:85], s[96:97] op_sel_hi:[1,0]
	v_pk_mul_f32 v[86:87], v[86:87], s[96:97] op_sel_hi:[1,0]
	v_exp_f32_e32 v80, v80
	v_exp_f32_e32 v81, v81
	v_exp_f32_e32 v82, v82
	v_pk_fma_f32 v[80:81], v[80:81], s[98:99], s[98:99] op_sel_hi:[1,0,0]
	v_exp_f32_e32 v83, v83
	v_exp_f32_e32 v84, v84
	v_pk_fma_f32 v[82:83], v[82:83], s[98:99], s[98:99] op_sel_hi:[1,0,0]
	v_exp_f32_e32 v85, v85
	v_exp_f32_e32 v86, v86
	v_pk_add_f32 v[84:85], v[84:85], 1.0 op_sel_hi:[1,0]
	v_exp_f32_e32 v87, v87
	v_pk_mul_f32 v[80:81], v[80:81], v[84:85]
	v_rcp_f32_e32 v80, v80
	v_pk_add_f32 v[86:87], v[86:87], 1.0 op_sel_hi:[1,0]
	v_rcp_f32_e32 v81, v81
	v_pk_mul_f32 v[82:83], v[82:83], v[86:87]
	v_pk_add_f32 v[84:85], v[84:85], 2.0 op_sel_hi:[1,0] neg_lo:[1,0] neg_hi:[1,0]
	v_rcp_f32_e32 v82, v82
	v_rcp_f32_e32 v83, v83
	v_pk_add_f32 v[86:87], v[86:87], 2.0 op_sel_hi:[1,0] neg_lo:[1,0] neg_hi:[1,0]
	v_pk_mul_f32 v[80:81], v[80:81], v[84:85]
	v_pk_mul_f32 v[82:83], v[82:83], v[86:87]
	v_ashrrev_i32_e32 v205, 31, v204
	v_cvt_pk_fp8_f32 v88, v80, v81
	s_and_b64 vcc, exec, s[0:1]
	v_cvt_pk_fp8_f32 v88, v82, v83 op_sel:[0,0,1]
	v_lshlrev_b64 v[84:85], 10, v[204:205]
	v_lshl_add_u64 v[86:87], v[122:123], 0, v[84:85]
	global_store_dword v[86:87], v88, off
	v_pk_mul_f32 v[80:81], v[80:81], s[98:99] op_sel_hi:[1,0]
	v_pk_mul_f32 v[82:83], v[82:83], s[98:99] op_sel_hi:[1,0]
	v_cvt_pk_f16_f32 v80, v80, v81
	v_cvt_pk_f16_f32 v81, v82, v83
	v_lshl_add_u64 v[82:83], v[84:85], 1, v[120:121]
	global_store_dwordx2 v[82:83], v[80:81], off
	v_exp_f32_e32 v72, v72
	v_exp_f32_e32 v73, v73
	v_exp_f32_e32 v74, v74
	v_pk_add_f32 v[72:73], v[72:73], 1.0 op_sel_hi:[1,0]
	v_exp_f32_e32 v75, v75
	v_exp_f32_e32 v76, v76
	v_pk_add_f32 v[74:75], v[74:75], 1.0 op_sel_hi:[1,0]
	v_exp_f32_e32 v77, v77
	v_exp_f32_e32 v78, v78
	v_pk_add_f32 v[76:77], v[76:77], 1.0 op_sel_hi:[1,0]
	v_exp_f32_e32 v79, v79
	v_exp_f32_e32 v68, v68
	v_pk_add_f32 v[78:79], v[78:79], 1.0 op_sel_hi:[1,0]
	v_exp_f32_e32 v69, v69
	v_pk_mul_f32 v[72:73], v[72:73], v[76:77]
	v_exp_f32_e32 v70, v70
	v_pk_mul_f32 v[74:75], v[74:75], v[78:79]
	v_exp_f32_e32 v71, v71
	v_pk_add_f32 v[68:69], v[68:69], 1.0 op_sel_hi:[1,0]
	v_rcp_f32_e32 v72, v72
	v_rcp_f32_e32 v73, v73
	v_pk_add_f32 v[70:71], v[70:71], 1.0 op_sel_hi:[1,0]
	v_rcp_f32_e32 v74, v74
	v_rcp_f32_e32 v75, v75
	v_pk_add_f32 v[76:77], v[76:77], 2.0 op_sel_hi:[1,0] neg_lo:[1,0] neg_hi:[1,0]
	v_rcp_f32_e32 v68, v68
	v_rcp_f32_e32 v69, v69
	v_pk_add_f32 v[78:79], v[78:79], 2.0 op_sel_hi:[1,0] neg_lo:[1,0] neg_hi:[1,0]
	v_rcp_f32_e32 v70, v70
	v_rcp_f32_e32 v71, v71
	v_pk_mul_f32 v[76:77], v[76:77], v[72:73]
	v_pk_mul_f32 v[78:79], v[78:79], v[74:75]
	s_waitcnt lgkmcnt(0)
	v_lshl_add_u64 v[72:73], v[176:177], 0, s[20:21]
	v_pk_fma_f32 v[68:69], v[160:161], v[68:69], v[76:77]
	v_pk_fma_f32 v[70:71], v[162:163], v[70:71], v[78:79]
	global_store_dwordx4 v[72:73], v[68:71], off sc1
	s_nop 1
	v_pk_mul_f32 v[68:69], v[68:69], s[96:97] op_sel_hi:[1,0]
	v_pk_mul_f32 v[70:71], v[70:71], s[96:97] op_sel_hi:[1,0]
	v_exp_f32_e32 v64, v64
	v_exp_f32_e32 v65, v65
	v_exp_f32_e32 v66, v66
	v_pk_fma_f32 v[64:65], v[64:65], s[98:99], s[98:99] op_sel_hi:[1,0,0]
	v_exp_f32_e32 v67, v67
	v_exp_f32_e32 v68, v68
	v_pk_fma_f32 v[66:67], v[66:67], s[98:99], s[98:99] op_sel_hi:[1,0,0]
	v_exp_f32_e32 v69, v69
	v_exp_f32_e32 v70, v70
	v_pk_add_f32 v[68:69], v[68:69], 1.0 op_sel_hi:[1,0]
	v_exp_f32_e32 v71, v71
	v_pk_mul_f32 v[64:65], v[64:65], v[68:69]
	v_rcp_f32_e32 v64, v64
	v_pk_add_f32 v[70:71], v[70:71], 1.0 op_sel_hi:[1,0]
	v_rcp_f32_e32 v65, v65
	v_pk_mul_f32 v[66:67], v[66:67], v[70:71]
	v_pk_add_f32 v[68:69], v[68:69], 2.0 op_sel_hi:[1,0] neg_lo:[1,0] neg_hi:[1,0]
	v_rcp_f32_e32 v66, v66
	v_rcp_f32_e32 v67, v67
	v_pk_add_f32 v[70:71], v[70:71], 2.0 op_sel_hi:[1,0] neg_lo:[1,0] neg_hi:[1,0]
	v_pk_mul_f32 v[64:65], v[64:65], v[68:69]
	v_pk_mul_f32 v[66:67], v[66:67], v[70:71]
	v_ashrrev_i32_e32 v203, 31, v202
	v_cvt_pk_fp8_f32 v72, v64, v65
	s_and_b64 vcc, exec, s[0:1]
	v_cvt_pk_fp8_f32 v72, v66, v67 op_sel:[0,0,1]
	v_lshlrev_b64 v[68:69], 10, v[202:203]
	v_lshl_add_u64 v[70:71], v[122:123], 0, v[68:69]
	global_store_dword v[70:71], v72, off
	v_pk_mul_f32 v[64:65], v[64:65], s[98:99] op_sel_hi:[1,0]
	v_pk_mul_f32 v[66:67], v[66:67], s[98:99] op_sel_hi:[1,0]
	v_cvt_pk_f16_f32 v64, v64, v65
	v_cvt_pk_f16_f32 v65, v66, v67
	v_lshl_add_u64 v[66:67], v[68:69], 1, v[120:121]
	global_store_dwordx2 v[66:67], v[64:65], off
	v_exp_f32_e32 v56, v56
	v_exp_f32_e32 v57, v57
	v_exp_f32_e32 v58, v58
	v_pk_add_f32 v[56:57], v[56:57], 1.0 op_sel_hi:[1,0]
	v_exp_f32_e32 v59, v59
	v_exp_f32_e32 v60, v60
	v_pk_add_f32 v[58:59], v[58:59], 1.0 op_sel_hi:[1,0]
	v_exp_f32_e32 v61, v61
	v_exp_f32_e32 v62, v62
	v_pk_add_f32 v[60:61], v[60:61], 1.0 op_sel_hi:[1,0]
	v_exp_f32_e32 v63, v63
	v_exp_f32_e32 v52, v52
	v_pk_add_f32 v[62:63], v[62:63], 1.0 op_sel_hi:[1,0]
	v_exp_f32_e32 v53, v53
	v_pk_mul_f32 v[56:57], v[56:57], v[60:61]
	v_exp_f32_e32 v54, v54
	v_pk_mul_f32 v[58:59], v[58:59], v[62:63]
	v_exp_f32_e32 v55, v55
	v_pk_add_f32 v[52:53], v[52:53], 1.0 op_sel_hi:[1,0]
	v_rcp_f32_e32 v56, v56
	v_rcp_f32_e32 v57, v57
	v_pk_add_f32 v[54:55], v[54:55], 1.0 op_sel_hi:[1,0]
	v_rcp_f32_e32 v58, v58
	v_rcp_f32_e32 v59, v59
	v_pk_add_f32 v[60:61], v[60:61], 2.0 op_sel_hi:[1,0] neg_lo:[1,0] neg_hi:[1,0]
	v_rcp_f32_e32 v52, v52
	v_rcp_f32_e32 v53, v53
	v_pk_add_f32 v[62:63], v[62:63], 2.0 op_sel_hi:[1,0] neg_lo:[1,0] neg_hi:[1,0]
	v_rcp_f32_e32 v54, v54
	v_rcp_f32_e32 v55, v55
	v_pk_mul_f32 v[60:61], v[60:61], v[56:57]
	v_pk_mul_f32 v[62:63], v[62:63], v[58:59]
	s_waitcnt vmcnt(8)
	v_pk_fma_f32 v[52:53], v[156:157], v[52:53], v[60:61]
	v_pk_fma_f32 v[54:55], v[158:159], v[54:55], v[62:63]
	v_lshl_add_u64 v[56:57], v[176:177], 0, s[14:15]
	global_store_dwordx4 v[56:57], v[52:55], off sc1
	s_nop 1
	v_pk_mul_f32 v[52:53], v[52:53], s[96:97] op_sel_hi:[1,0]
	v_pk_mul_f32 v[54:55], v[54:55], s[96:97] op_sel_hi:[1,0]
	v_exp_f32_e32 v48, v48
	v_exp_f32_e32 v49, v49
	v_exp_f32_e32 v50, v50
	v_pk_fma_f32 v[48:49], v[48:49], s[98:99], s[98:99] op_sel_hi:[1,0,0]
	v_exp_f32_e32 v51, v51
	v_exp_f32_e32 v52, v52
	v_pk_fma_f32 v[50:51], v[50:51], s[98:99], s[98:99] op_sel_hi:[1,0,0]
	v_exp_f32_e32 v53, v53
	v_exp_f32_e32 v54, v54
	v_pk_add_f32 v[52:53], v[52:53], 1.0 op_sel_hi:[1,0]
	v_exp_f32_e32 v55, v55
	v_pk_mul_f32 v[48:49], v[48:49], v[52:53]
	v_rcp_f32_e32 v48, v48
	v_pk_add_f32 v[54:55], v[54:55], 1.0 op_sel_hi:[1,0]
	v_rcp_f32_e32 v49, v49
	v_pk_mul_f32 v[50:51], v[50:51], v[54:55]
	v_pk_add_f32 v[52:53], v[52:53], 2.0 op_sel_hi:[1,0] neg_lo:[1,0] neg_hi:[1,0]
	v_rcp_f32_e32 v50, v50
	v_rcp_f32_e32 v51, v51
	v_pk_add_f32 v[54:55], v[54:55], 2.0 op_sel_hi:[1,0] neg_lo:[1,0] neg_hi:[1,0]
	v_pk_mul_f32 v[48:49], v[48:49], v[52:53]
	v_pk_mul_f32 v[50:51], v[50:51], v[54:55]
	v_ashrrev_i32_e32 v201, 31, v200
	v_cvt_pk_fp8_f32 v56, v48, v49
	s_and_b64 vcc, exec, s[0:1]
	v_cvt_pk_fp8_f32 v56, v50, v51 op_sel:[0,0,1]
	v_lshlrev_b64 v[52:53], 10, v[200:201]
	v_lshl_add_u64 v[54:55], v[122:123], 0, v[52:53]
	global_store_dword v[54:55], v56, off
	v_pk_mul_f32 v[48:49], v[48:49], s[98:99] op_sel_hi:[1,0]
	v_pk_mul_f32 v[50:51], v[50:51], s[98:99] op_sel_hi:[1,0]
	v_cvt_pk_f16_f32 v48, v48, v49
	v_cvt_pk_f16_f32 v49, v50, v51
	v_lshl_add_u64 v[50:51], v[52:53], 1, v[120:121]
	global_store_dwordx2 v[50:51], v[48:49], off
	v_exp_f32_e32 v40, v40
	v_exp_f32_e32 v41, v41
	v_exp_f32_e32 v42, v42
	v_pk_add_f32 v[40:41], v[40:41], 1.0 op_sel_hi:[1,0]
	v_exp_f32_e32 v43, v43
	v_exp_f32_e32 v44, v44
	v_pk_add_f32 v[42:43], v[42:43], 1.0 op_sel_hi:[1,0]
	v_exp_f32_e32 v45, v45
	v_exp_f32_e32 v46, v46
	v_pk_add_f32 v[44:45], v[44:45], 1.0 op_sel_hi:[1,0]
	v_exp_f32_e32 v47, v47
	v_exp_f32_e32 v36, v36
	v_pk_add_f32 v[46:47], v[46:47], 1.0 op_sel_hi:[1,0]
	v_exp_f32_e32 v37, v37
	v_pk_mul_f32 v[40:41], v[40:41], v[44:45]
	v_exp_f32_e32 v38, v38
	v_pk_mul_f32 v[42:43], v[42:43], v[46:47]
	v_exp_f32_e32 v39, v39
	v_pk_add_f32 v[36:37], v[36:37], 1.0 op_sel_hi:[1,0]
	v_rcp_f32_e32 v40, v40
	v_rcp_f32_e32 v41, v41
	v_pk_add_f32 v[38:39], v[38:39], 1.0 op_sel_hi:[1,0]
	v_rcp_f32_e32 v42, v42
	v_rcp_f32_e32 v43, v43
	v_pk_add_f32 v[44:45], v[44:45], 2.0 op_sel_hi:[1,0] neg_lo:[1,0] neg_hi:[1,0]
	v_rcp_f32_e32 v36, v36
	v_rcp_f32_e32 v37, v37
	v_pk_add_f32 v[46:47], v[46:47], 2.0 op_sel_hi:[1,0] neg_lo:[1,0] neg_hi:[1,0]
	v_rcp_f32_e32 v38, v38
	v_rcp_f32_e32 v39, v39
	v_pk_mul_f32 v[44:45], v[44:45], v[40:41]
	v_pk_mul_f32 v[46:47], v[46:47], v[42:43]
	v_lshl_add_u64 v[40:41], v[176:177], 0, s[22:23]
	v_pk_fma_f32 v[36:37], v[152:153], v[36:37], v[44:45]
	v_pk_fma_f32 v[38:39], v[154:155], v[38:39], v[46:47]
	global_store_dwordx4 v[40:41], v[36:39], off sc1
	s_nop 1
	v_pk_mul_f32 v[36:37], v[36:37], s[96:97] op_sel_hi:[1,0]
	v_pk_mul_f32 v[38:39], v[38:39], s[96:97] op_sel_hi:[1,0]
	v_exp_f32_e32 v32, v32
	v_exp_f32_e32 v33, v33
	v_exp_f32_e32 v34, v34
	v_pk_fma_f32 v[32:33], v[32:33], s[98:99], s[98:99] op_sel_hi:[1,0,0]
	v_exp_f32_e32 v35, v35
	v_exp_f32_e32 v36, v36
	v_pk_fma_f32 v[34:35], v[34:35], s[98:99], s[98:99] op_sel_hi:[1,0,0]
	v_exp_f32_e32 v37, v37
	v_exp_f32_e32 v38, v38
	v_pk_add_f32 v[36:37], v[36:37], 1.0 op_sel_hi:[1,0]
	v_exp_f32_e32 v39, v39
	v_pk_mul_f32 v[32:33], v[32:33], v[36:37]
	v_rcp_f32_e32 v32, v32
	v_pk_add_f32 v[38:39], v[38:39], 1.0 op_sel_hi:[1,0]
	v_rcp_f32_e32 v33, v33
	v_pk_mul_f32 v[34:35], v[34:35], v[38:39]
	v_pk_add_f32 v[36:37], v[36:37], 2.0 op_sel_hi:[1,0] neg_lo:[1,0] neg_hi:[1,0]
	v_rcp_f32_e32 v34, v34
	v_rcp_f32_e32 v35, v35
	v_pk_add_f32 v[38:39], v[38:39], 2.0 op_sel_hi:[1,0] neg_lo:[1,0] neg_hi:[1,0]
	v_pk_mul_f32 v[32:33], v[32:33], v[36:37]
	v_pk_mul_f32 v[34:35], v[34:35], v[38:39]
	v_cvt_pk_fp8_f32 v40, v32, v33
	v_or_b32_e32 v36, 16, v200
	v_ashrrev_i32_e32 v37, 31, v36
	v_lshlrev_b64 v[36:37], 10, v[36:37]
	v_cvt_pk_fp8_f32 v40, v34, v35 op_sel:[0,0,1]
	v_lshl_add_u64 v[38:39], v[122:123], 0, v[36:37]
	global_store_dword v[38:39], v40, off
	v_pk_mul_f32 v[32:33], v[32:33], s[98:99] op_sel_hi:[1,0]
	v_pk_mul_f32 v[34:35], v[34:35], s[98:99] op_sel_hi:[1,0]
	v_cvt_pk_f16_f32 v32, v32, v33
	v_cvt_pk_f16_f32 v33, v34, v35
	v_lshl_add_u64 v[34:35], v[36:37], 1, v[120:121]
	global_store_dwordx2 v[34:35], v[32:33], off
	v_exp_f32_e32 v24, v24
	v_exp_f32_e32 v25, v25
	v_exp_f32_e32 v26, v26
	v_pk_add_f32 v[24:25], v[24:25], 1.0 op_sel_hi:[1,0]
	v_exp_f32_e32 v27, v27
	v_exp_f32_e32 v28, v28
	v_pk_add_f32 v[26:27], v[26:27], 1.0 op_sel_hi:[1,0]
	v_exp_f32_e32 v29, v29
	v_exp_f32_e32 v30, v30
	v_pk_add_f32 v[28:29], v[28:29], 1.0 op_sel_hi:[1,0]
	v_exp_f32_e32 v31, v31
	v_exp_f32_e32 v20, v20
	v_pk_add_f32 v[30:31], v[30:31], 1.0 op_sel_hi:[1,0]
	v_exp_f32_e32 v21, v21
	v_pk_mul_f32 v[24:25], v[24:25], v[28:29]
	v_exp_f32_e32 v22, v22
	v_pk_mul_f32 v[26:27], v[26:27], v[30:31]
	v_exp_f32_e32 v23, v23
	v_pk_add_f32 v[20:21], v[20:21], 1.0 op_sel_hi:[1,0]
	v_rcp_f32_e32 v24, v24
	v_rcp_f32_e32 v25, v25
	v_pk_add_f32 v[22:23], v[22:23], 1.0 op_sel_hi:[1,0]
	v_rcp_f32_e32 v26, v26
	v_rcp_f32_e32 v27, v27
	v_pk_add_f32 v[28:29], v[28:29], 2.0 op_sel_hi:[1,0] neg_lo:[1,0] neg_hi:[1,0]
	v_rcp_f32_e32 v20, v20
	v_rcp_f32_e32 v21, v21
	v_pk_add_f32 v[30:31], v[30:31], 2.0 op_sel_hi:[1,0] neg_lo:[1,0] neg_hi:[1,0]
	v_rcp_f32_e32 v22, v22
	v_rcp_f32_e32 v23, v23
	v_pk_mul_f32 v[28:29], v[28:29], v[24:25]
	v_pk_mul_f32 v[30:31], v[30:31], v[26:27]
	v_pk_fma_f32 v[20:21], v[148:149], v[20:21], v[28:29]
	v_pk_fma_f32 v[22:23], v[150:151], v[22:23], v[30:31]
	v_lshl_add_u64 v[24:25], v[176:177], 0, s[16:17]
	global_store_dwordx4 v[24:25], v[20:23], off sc1
	s_nop 1
	v_pk_mul_f32 v[20:21], v[20:21], s[96:97] op_sel_hi:[1,0]
	v_pk_mul_f32 v[22:23], v[22:23], s[96:97] op_sel_hi:[1,0]
	v_exp_f32_e32 v16, v16
	v_exp_f32_e32 v17, v17
	v_exp_f32_e32 v18, v18
	v_pk_fma_f32 v[16:17], v[16:17], s[98:99], s[98:99] op_sel_hi:[1,0,0]
	v_exp_f32_e32 v19, v19
	v_exp_f32_e32 v20, v20
	v_pk_fma_f32 v[18:19], v[18:19], s[98:99], s[98:99] op_sel_hi:[1,0,0]
	v_exp_f32_e32 v21, v21
	v_exp_f32_e32 v22, v22
	v_pk_add_f32 v[20:21], v[20:21], 1.0 op_sel_hi:[1,0]
	v_exp_f32_e32 v23, v23
	v_pk_mul_f32 v[16:17], v[16:17], v[20:21]
	v_rcp_f32_e32 v16, v16
	v_pk_add_f32 v[22:23], v[22:23], 1.0 op_sel_hi:[1,0]
	v_rcp_f32_e32 v17, v17
	v_pk_mul_f32 v[18:19], v[18:19], v[22:23]
	v_pk_add_f32 v[20:21], v[20:21], 2.0 op_sel_hi:[1,0] neg_lo:[1,0] neg_hi:[1,0]
	v_rcp_f32_e32 v18, v18
	v_rcp_f32_e32 v19, v19
	v_pk_add_f32 v[22:23], v[22:23], 2.0 op_sel_hi:[1,0] neg_lo:[1,0] neg_hi:[1,0]
	v_pk_mul_f32 v[16:17], v[16:17], v[20:21]
	v_pk_mul_f32 v[18:19], v[18:19], v[22:23]
	v_cvt_pk_fp8_f32 v24, v16, v17
	v_or_b32_e32 v20, 32, v200
	v_ashrrev_i32_e32 v21, 31, v20
	v_lshlrev_b64 v[20:21], 10, v[20:21]
	v_cvt_pk_fp8_f32 v24, v18, v19 op_sel:[0,0,1]
	v_lshl_add_u64 v[22:23], v[122:123], 0, v[20:21]
	global_store_dword v[22:23], v24, off
	v_pk_mul_f32 v[16:17], v[16:17], s[98:99] op_sel_hi:[1,0]
	v_pk_mul_f32 v[18:19], v[18:19], s[98:99] op_sel_hi:[1,0]
	v_cvt_pk_f16_f32 v16, v16, v17
	v_cvt_pk_f16_f32 v17, v18, v19
	v_lshl_add_u64 v[18:19], v[20:21], 1, v[120:121]
	global_store_dwordx2 v[18:19], v[16:17], off
	v_exp_f32_e32 v8, v8
	v_exp_f32_e32 v9, v9
	v_exp_f32_e32 v10, v10
	v_pk_add_f32 v[8:9], v[8:9], 1.0 op_sel_hi:[1,0]
	v_exp_f32_e32 v11, v11
	v_exp_f32_e32 v12, v12
	v_pk_add_f32 v[10:11], v[10:11], 1.0 op_sel_hi:[1,0]
	v_exp_f32_e32 v13, v13
	v_exp_f32_e32 v14, v14
	v_pk_add_f32 v[12:13], v[12:13], 1.0 op_sel_hi:[1,0]
	v_exp_f32_e32 v15, v15
	v_exp_f32_e32 v4, v4
	v_pk_add_f32 v[14:15], v[14:15], 1.0 op_sel_hi:[1,0]
	v_exp_f32_e32 v5, v5
	v_pk_mul_f32 v[8:9], v[8:9], v[12:13]
	v_exp_f32_e32 v6, v6
	v_pk_mul_f32 v[10:11], v[10:11], v[14:15]
	v_exp_f32_e32 v7, v7
	v_pk_add_f32 v[4:5], v[4:5], 1.0 op_sel_hi:[1,0]
	v_rcp_f32_e32 v8, v8
	v_rcp_f32_e32 v9, v9
	v_pk_add_f32 v[6:7], v[6:7], 1.0 op_sel_hi:[1,0]
	v_rcp_f32_e32 v10, v10
	v_rcp_f32_e32 v11, v11
	v_pk_add_f32 v[12:13], v[12:13], 2.0 op_sel_hi:[1,0] neg_lo:[1,0] neg_hi:[1,0]
	v_rcp_f32_e32 v4, v4
	v_rcp_f32_e32 v5, v5
	v_pk_add_f32 v[14:15], v[14:15], 2.0 op_sel_hi:[1,0] neg_lo:[1,0] neg_hi:[1,0]
	v_rcp_f32_e32 v6, v6
	v_rcp_f32_e32 v7, v7
	v_pk_mul_f32 v[12:13], v[12:13], v[8:9]
	v_pk_mul_f32 v[14:15], v[14:15], v[10:11]
	v_lshl_add_u64 v[8:9], v[176:177], 0, s[24:25]
	v_pk_fma_f32 v[4:5], v[144:145], v[4:5], v[12:13]
	v_pk_fma_f32 v[6:7], v[146:147], v[6:7], v[14:15]
	global_store_dwordx4 v[8:9], v[4:7], off sc1
	s_nop 1
	v_pk_mul_f32 v[4:5], v[4:5], s[96:97] op_sel_hi:[1,0]
	v_pk_mul_f32 v[6:7], v[6:7], s[96:97] op_sel_hi:[1,0]
	v_exp_f32_e32 v0, v0
	v_exp_f32_e32 v1, v1
	v_exp_f32_e32 v2, v2
	v_pk_fma_f32 v[0:1], v[0:1], s[98:99], s[98:99] op_sel_hi:[1,0,0]
	v_exp_f32_e32 v3, v3
	v_exp_f32_e32 v4, v4
	v_pk_fma_f32 v[2:3], v[2:3], s[98:99], s[98:99] op_sel_hi:[1,0,0]
	v_exp_f32_e32 v5, v5
	v_exp_f32_e32 v6, v6
	v_pk_add_f32 v[4:5], v[4:5], 1.0 op_sel_hi:[1,0]
	v_exp_f32_e32 v7, v7
	v_pk_mul_f32 v[0:1], v[0:1], v[4:5]
	v_rcp_f32_e32 v0, v0
	v_pk_add_f32 v[6:7], v[6:7], 1.0 op_sel_hi:[1,0]
	v_rcp_f32_e32 v1, v1
	v_pk_mul_f32 v[2:3], v[2:3], v[6:7]
	v_pk_add_f32 v[4:5], v[4:5], 2.0 op_sel_hi:[1,0] neg_lo:[1,0] neg_hi:[1,0]
	v_rcp_f32_e32 v2, v2
	v_rcp_f32_e32 v3, v3
	v_pk_add_f32 v[6:7], v[6:7], 2.0 op_sel_hi:[1,0] neg_lo:[1,0] neg_hi:[1,0]
	v_pk_mul_f32 v[0:1], v[0:1], v[4:5]
	v_pk_mul_f32 v[2:3], v[2:3], v[6:7]
	v_cvt_pk_fp8_f32 v8, v0, v1
	v_or_b32_e32 v4, 48, v200
	v_ashrrev_i32_e32 v5, 31, v4
	v_lshlrev_b64 v[4:5], 10, v[4:5]
	v_cvt_pk_fp8_f32 v8, v2, v3 op_sel:[0,0,1]
	v_lshl_add_u64 v[6:7], v[122:123], 0, v[4:5]
	global_store_dword v[6:7], v8, off
	v_pk_mul_f32 v[0:1], v[0:1], s[98:99] op_sel_hi:[1,0]
	v_pk_mul_f32 v[2:3], v[2:3], s[98:99] op_sel_hi:[1,0]
	v_cvt_pk_f16_f32 v0, v0, v1
	v_cvt_pk_f16_f32 v1, v2, v3
	v_lshl_add_u64 v[2:3], v[4:5], 1, v[120:121]
	global_store_dwordx2 v[2:3], v[0:1], off
	s_branch .LBB2_24
